# speedup vs baseline: 1.0223x; 1.0223x over previous
_Z10k_final_lnPKDF16_PKDv2_fPKfS5_Pf:
	v_lshl_or_b32 v6, s2, 8, v0
	s_mov_b32 s3, 0x55555556
	v_mul_hi_u32 v0, v6, s3
	v_mov_b32_e32 v1, 0
	s_lshr_b32 s12, s2, 24
	v_mov_b32_e32 v2, 0x55555556
	v_mad_u64_u32 v[2:3], s[2:3], s12, v2, v[0:1]
	v_mov_b32_e32 v0, v2
	s_mov_b32 s2, 0x1555555
	v_mad_u64_u32 v[4:5], s[2:3], v6, s2, v[0:1]
	v_mov_b32_e32 v0, v5
	v_mov_b32_e32 v2, v3
	v_mov_b32_e32 v3, v1
	s_load_dwordx8 s[4:11], s[0:1], 0x0
	v_lshl_add_u64 v[0:1], v[2:3], 0, v[0:1]
	v_mov_b32_e32 v2, 0x1555555
	v_mad_u64_u32 v[0:1], s[2:3], s12, v2, v[0:1]
	s_movk_i32 s2, 0xff40
	s_nop 0
	v_mul_lo_u32 v1, v0, s2
	s_movk_i32 s2, 0x300
	v_add_lshl_u32 v2, v1, v6, 2
	v_mad_i64_i32 v[8:9], s[2:3], v0, s2, 0
	s_waitcnt lgkmcnt(0)
	v_lshl_add_u64 v[4:5], v[8:9], 1, s[4:5]
	v_ashrrev_i32_e32 v3, 31, v2
	v_lshl_add_u64 v[4:5], v[2:3], 1, v[4:5]
	global_load_dwordx2 v[10:11], v[4:5], off nt
	v_ashrrev_i32_e32 v1, 31, v0
	v_lshl_add_u64 v[0:1], v[0:1], 3, s[6:7]
	global_load_dwordx2 v[12:13], v[0:1], off
	v_lshlrev_b64 v[14:15], 2, v[2:3]
	v_lshl_add_u64 v[0:1], s[8:9], 0, v[14:15]
	v_lshl_add_u64 v[4:5], s[10:11], 0, v[14:15]
	global_load_dwordx4 v[0:3], v[0:1], off
	s_load_dwordx2 s[0:1], s[0:1], 0x20
	global_load_dwordx4 v[4:7], v[4:5], off
	s_waitcnt lgkmcnt(0)
	v_lshl_add_u64 v[8:9], v[8:9], 2, s[0:1]
	s_waitcnt vmcnt(3)
	v_cvt_f32_f16_e32 v16, v11
	v_cvt_f32_f16_sdwa v11, v11 dst_sel:DWORD dst_unused:UNUSED_PAD src0_sel:WORD_1
	v_cvt_f32_f16_e32 v17, v10
	v_cvt_f32_f16_sdwa v18, v10 dst_sel:DWORD dst_unused:UNUSED_PAD src0_sel:WORD_1
	s_waitcnt vmcnt(2)
	v_sub_f32_e32 v10, v16, v12
	v_sub_f32_e32 v11, v11, v12
	v_sub_f32_e32 v16, v17, v12
	v_sub_f32_e32 v17, v18, v12
	v_pk_mul_f32 v[16:17], v[12:13], v[16:17] op_sel:[1,0]
	v_pk_mul_f32 v[10:11], v[12:13], v[10:11] op_sel:[1,0]
	s_waitcnt vmcnt(0)
	v_pk_fma_f32 v[0:1], v[0:1], v[16:17], v[4:5]
	v_pk_fma_f32 v[2:3], v[2:3], v[10:11], v[6:7]
	v_lshl_add_u64 v[4:5], v[8:9], 0, v[14:15]
	global_store_dwordx4 v[4:5], v[0:3], off nt
	s_endpgm
	s_endpgm
	s_endpgm
	s_endpgm
	s_endpgm
	s_endpgm
	s_endpgm
	s_endpgm
	s_endpgm
	s_endpgm
	s_endpgm
	s_endpgm
	s_endpgm
	s_endpgm
	s_endpgm
	s_endpgm
	s_endpgm
	s_endpgm
	s_endpgm
	s_endpgm
	s_endpgm
	s_endpgm
	s_endpgm
	s_endpgm
	s_endpgm
	s_endpgm
	s_endpgm
	s_endpgm
	s_endpgm
	s_endpgm
	s_endpgm
	s_endpgm
	s_endpgm
	s_endpgm
	s_endpgm
	s_endpgm
	s_endpgm
	s_endpgm

.LBB7_26:
	s_lshl_b32 s34, s70, 8
	s_add_i32 s34, s34, s48
	v_or_b32_e32 v250, s34, v165
	v_ashrrev_i32_e32 v251, 31, v250
	v_lshl_add_u64 v[250:251], v[250:251], 3, s[12:13]
	s_lshl_b32 s35, s67, 8
	s_or_b32 s35, s35, s51
	v_or_b32_e32 v252, s35, v164
	v_ashrrev_i32_e32 v253, 31, v252
	v_lshl_add_u64 v[252:253], v[252:253], 2, s[14:15]
	global_load_dword v226, v[250:251], off offset:4
	global_load_dword v227, v[250:251], off offset:132
	global_load_dword v228, v[250:251], off offset:260
	global_load_dword v229, v[250:251], off offset:388
	global_load_dword v230, v[250:251], off offset:1028
	global_load_dword v231, v[250:251], off offset:1156
	global_load_dword v232, v[250:251], off offset:1284
	global_load_dword v233, v[250:251], off offset:1412
	global_load_dwordx4 v[234:237], v[252:253], off
	global_load_dwordx4 v[238:241], v[252:253], off offset:16
	global_load_dwordx4 v[242:245], v[252:253], off offset:128
	global_load_dwordx4 v[246:249], v[252:253], off offset:144
	s_add_u32 s28, s28, 0x30080
	s_addc_u32 s29, s29, 0
	s_add_u32 s71, s30, 0x100
	v_mov_b32_e32 v0, 0
	s_addc_u32 s72, s31, 0
	s_mov_b32 s73, -2
	v_mov_b32_e32 v1, v0
	v_mov_b32_e32 v2, v0
	v_mov_b32_e32 v3, v0
	v_mov_b32_e32 v4, v0
	v_mov_b32_e32 v5, v0
	v_mov_b32_e32 v6, v0
	v_mov_b32_e32 v7, v0
	v_mov_b32_e32 v12, v0
	v_mov_b32_e32 v13, v0
	v_mov_b32_e32 v14, v0
	v_mov_b32_e32 v15, v0
	v_mov_b32_e32 v20, v0
	v_mov_b32_e32 v21, v0
	v_mov_b32_e32 v22, v0
	v_mov_b32_e32 v23, v0
	v_mov_b32_e32 v28, v0
	v_mov_b32_e32 v29, v0
	v_mov_b32_e32 v30, v0
	v_mov_b32_e32 v31, v0
	v_mov_b32_e32 v36, v0
	v_mov_b32_e32 v37, v0
	v_mov_b32_e32 v38, v0
	v_mov_b32_e32 v39, v0
	v_mov_b32_e32 v44, v0
	v_mov_b32_e32 v45, v0
	v_mov_b32_e32 v46, v0
	v_mov_b32_e32 v47, v0
	v_mov_b32_e32 v52, v0
	v_mov_b32_e32 v53, v0
	v_mov_b32_e32 v54, v0
	v_mov_b32_e32 v55, v0
	v_mov_b32_e32 v8, v0
	v_mov_b32_e32 v9, v0
	v_mov_b32_e32 v10, v0
	v_mov_b32_e32 v11, v0
	v_mov_b32_e32 v16, v0
	v_mov_b32_e32 v17, v0
	v_mov_b32_e32 v18, v0
	v_mov_b32_e32 v19, v0
	v_mov_b32_e32 v24, v0
	v_mov_b32_e32 v25, v0
	v_mov_b32_e32 v26, v0
	v_mov_b32_e32 v27, v0
	v_mov_b32_e32 v32, v0
	v_mov_b32_e32 v33, v0
	v_mov_b32_e32 v34, v0
	v_mov_b32_e32 v35, v0
	v_mov_b32_e32 v40, v0
	v_mov_b32_e32 v41, v0
	v_mov_b32_e32 v42, v0
	v_mov_b32_e32 v43, v0
	v_mov_b32_e32 v48, v0
	v_mov_b32_e32 v49, v0
	v_mov_b32_e32 v50, v0
	v_mov_b32_e32 v51, v0
	v_mov_b32_e32 v56, v0
	v_mov_b32_e32 v57, v0
	v_mov_b32_e32 v58, v0
	v_mov_b32_e32 v59, v0
	v_mov_b32_e32 v60, v0
	v_mov_b32_e32 v61, v0
	v_mov_b32_e32 v62, v0
	v_mov_b32_e32 v63, v0
	v_mov_b32_e32 v64, v0
	v_mov_b32_e32 v65, v0
	v_mov_b32_e32 v66, v0
	v_mov_b32_e32 v67, v0
	v_mov_b32_e32 v68, v0
	v_mov_b32_e32 v69, v0
	v_mov_b32_e32 v70, v0
	v_mov_b32_e32 v71, v0
	v_mov_b32_e32 v76, v0
	v_mov_b32_e32 v77, v0
	v_mov_b32_e32 v78, v0
	v_mov_b32_e32 v79, v0
	v_mov_b32_e32 v84, v0
	v_mov_b32_e32 v85, v0
	v_mov_b32_e32 v86, v0
	v_mov_b32_e32 v87, v0
	v_mov_b32_e32 v92, v0
	v_mov_b32_e32 v93, v0
	v_mov_b32_e32 v94, v0
	v_mov_b32_e32 v95, v0
	v_mov_b32_e32 v100, v0
	v_mov_b32_e32 v101, v0
	v_mov_b32_e32 v102, v0
	v_mov_b32_e32 v103, v0
	v_mov_b32_e32 v112, v0
	v_mov_b32_e32 v113, v0
	v_mov_b32_e32 v114, v0
	v_mov_b32_e32 v115, v0
	v_mov_b32_e32 v116, v0
	v_mov_b32_e32 v117, v0
	v_mov_b32_e32 v118, v0
	v_mov_b32_e32 v119, v0
	v_mov_b32_e32 v72, v0
	v_mov_b32_e32 v73, v0
	v_mov_b32_e32 v74, v0
	v_mov_b32_e32 v75, v0
	v_mov_b32_e32 v80, v0
	v_mov_b32_e32 v81, v0
	v_mov_b32_e32 v82, v0
	v_mov_b32_e32 v83, v0
	v_mov_b32_e32 v88, v0
	v_mov_b32_e32 v89, v0
	v_mov_b32_e32 v90, v0
	v_mov_b32_e32 v91, v0
	v_mov_b32_e32 v96, v0
	v_mov_b32_e32 v97, v0
	v_mov_b32_e32 v98, v0
	v_mov_b32_e32 v99, v0
	v_mov_b32_e32 v104, v0
	v_mov_b32_e32 v105, v0
	v_mov_b32_e32 v106, v0
	v_mov_b32_e32 v107, v0
	v_mov_b32_e32 v108, v0
	v_mov_b32_e32 v109, v0
	v_mov_b32_e32 v110, v0
	v_mov_b32_e32 v111, v0
	v_mov_b32_e32 v120, v0
	v_mov_b32_e32 v121, v0
	v_mov_b32_e32 v122, v0
	v_mov_b32_e32 v123, v0
	v_mov_b32_e32 v124, v0
	v_mov_b32_e32 v125, v0
	v_mov_b32_e32 v126, v0
	v_mov_b32_e32 v127, v0
.LBB7_27:
	ds_read_b128 v[128:131], v170
	ds_read_b128 v[132:135], v170 offset:1024
	ds_read_b128 v[136:139], v170 offset:2048
	ds_read_b128 v[140:143], v170 offset:3072
	s_add_u32 s30, s28, 0xfffd0080
	s_addc_u32 s31, s29, -1
	s_cmp_eq_u32 s73, 8
	s_cselect_b32 s35, s9, s31
	s_cselect_b32 s34, s8, s30
	s_cselect_b32 s31, s1, s72
	s_cselect_b32 s30, s0, s71
	v_lshl_add_u64 v[162:163], s[28:29], 0, v[152:153]
	s_add_i32 m0, s43, 0xc000
	ds_read_b128 v[158:161], v171
	ds_read_b128 v[176:179], v171 offset:1024
	ds_read_b128 v[180:183], v171 offset:2048
	ds_read_b128 v[184:187], v171 offset:3072
	ds_read_b128 v[188:191], v171 offset:4096
	ds_read_b128 v[192:195], v171 offset:5120
	ds_read_b128 v[196:199], v171 offset:6144
	ds_read_b128 v[200:203], v171 offset:7168
	global_load_lds_dwordx4 v[162:163], off
	v_lshl_add_u64 v[162:163], s[28:29], 0, v[154:155]
	s_add_i32 m0, s43, 0xe000
	s_nop 0
	global_load_lds_dwordx4 v[162:163], off
	s_waitcnt lgkmcnt(8)
	s_barrier
	s_waitcnt lgkmcnt(0)
	s_setprio 1
	s_waitcnt lgkmcnt(0)
	v_mfma_f32_16x16x32_f16 v[124:127], v[128:131], v[158:161], v[124:127]
	v_mfma_f32_16x16x32_f16 v[120:123], v[136:139], v[158:161], v[120:123]
	v_mfma_f32_16x16x32_f16 v[108:111], v[128:131], v[180:183], v[108:111]
	v_mfma_f32_16x16x32_f16 v[104:107], v[136:139], v[180:183], v[104:107]
	v_mfma_f32_16x16x32_f16 v[96:99], v[128:131], v[188:191], v[96:99]
	v_mfma_f32_16x16x32_f16 v[88:91], v[136:139], v[188:191], v[88:91]
	v_mfma_f32_16x16x32_f16 v[80:83], v[128:131], v[196:199], v[80:83]
	v_mfma_f32_16x16x32_f16 v[72:75], v[136:139], v[196:199], v[72:75]
	v_mfma_f32_16x16x32_f16 v[124:127], v[132:135], v[176:179], v[124:127]
	v_mfma_f32_16x16x32_f16 v[120:123], v[140:143], v[176:179], v[120:123]
	v_mfma_f32_16x16x32_f16 v[108:111], v[132:135], v[184:187], v[108:111]
	v_mfma_f32_16x16x32_f16 v[104:107], v[140:143], v[184:187], v[104:107]
	v_mfma_f32_16x16x32_f16 v[96:99], v[132:135], v[192:195], v[96:99]
	v_mfma_f32_16x16x32_f16 v[88:91], v[140:143], v[192:195], v[88:91]
	v_mfma_f32_16x16x32_f16 v[80:83], v[132:135], v[200:203], v[80:83]
	v_mfma_f32_16x16x32_f16 v[72:75], v[140:143], v[200:203], v[72:75]
	s_setprio 0
	s_barrier
	s_add_i32 s74, s65, s42
	v_lshl_add_u64 v[162:163], s[30:31], 0, v[146:147]
	s_mov_b32 m0, s74
	ds_read_b128 v[204:207], v172
	ds_read_b128 v[208:211], v172 offset:1024
	ds_read_b128 v[212:215], v172 offset:2048
	ds_read_b128 v[216:219], v172 offset:3072
	global_load_lds_dwordx4 v[162:163], off
	v_lshl_add_u64 v[220:221], s[30:31], 0, v[150:151]
	s_add_i32 m0, s74, 0x2000
	s_nop 0
	global_load_lds_dwordx4 v[220:221], off
	s_barrier
	s_waitcnt lgkmcnt(0)
	s_setprio 1
	s_waitcnt lgkmcnt(0)
	v_mfma_f32_16x16x32_f16 v[116:119], v[204:207], v[158:161], v[116:119]
	v_mfma_f32_16x16x32_f16 v[112:115], v[212:215], v[158:161], v[112:115]
	v_mfma_f32_16x16x32_f16 v[100:103], v[204:207], v[180:183], v[100:103]
	v_mfma_f32_16x16x32_f16 v[92:95], v[212:215], v[180:183], v[92:95]
	v_mfma_f32_16x16x32_f16 v[84:87], v[204:207], v[188:191], v[84:87]
	v_mfma_f32_16x16x32_f16 v[76:79], v[212:215], v[188:191], v[76:79]
	v_mfma_f32_16x16x32_f16 v[68:71], v[204:207], v[196:199], v[68:71]
	v_mfma_f32_16x16x32_f16 v[64:67], v[212:215], v[196:199], v[64:67]
	v_mfma_f32_16x16x32_f16 v[116:119], v[208:211], v[176:179], v[116:119]
	v_mfma_f32_16x16x32_f16 v[112:115], v[216:219], v[176:179], v[112:115]
	v_mfma_f32_16x16x32_f16 v[100:103], v[208:211], v[184:187], v[100:103]
	v_mfma_f32_16x16x32_f16 v[92:95], v[216:219], v[184:187], v[92:95]
	v_mfma_f32_16x16x32_f16 v[84:87], v[208:211], v[192:195], v[84:87]
	v_mfma_f32_16x16x32_f16 v[76:79], v[216:219], v[192:195], v[76:79]
	v_mfma_f32_16x16x32_f16 v[68:71], v[208:211], v[200:203], v[68:71]
	v_mfma_f32_16x16x32_f16 v[64:67], v[216:219], v[200:203], v[64:67]
	s_setprio 0
	s_mov_b32 m0, s43
	v_lshl_add_u64 v[222:223], s[34:35], 0, v[144:145]
	s_barrier
	ds_read_b128 v[158:161], v171 offset:16384
	ds_read_b128 v[176:179], v171 offset:17408
	ds_read_b128 v[180:183], v171 offset:18432
	ds_read_b128 v[184:187], v171 offset:19456
	ds_read_b128 v[188:191], v171 offset:20480
	ds_read_b128 v[192:195], v171 offset:21504
	ds_read_b128 v[196:199], v171 offset:22528
	ds_read_b128 v[200:203], v171 offset:23552
	global_load_lds_dwordx4 v[222:223], off
	v_lshl_add_u64 v[224:225], s[34:35], 0, v[148:149]
	s_mov_b32 m0, s44
	s_nop 0
	global_load_lds_dwordx4 v[224:225], off
	s_barrier
	s_waitcnt lgkmcnt(0)
	s_setprio 1
	s_waitcnt lgkmcnt(0)
	v_mfma_f32_16x16x32_f16 v[60:63], v[128:131], v[158:161], v[60:63]
	v_mfma_f32_16x16x32_f16 v[56:59], v[136:139], v[158:161], v[56:59]
	v_mfma_f32_16x16x32_f16 v[48:51], v[128:131], v[180:183], v[48:51]
	v_mfma_f32_16x16x32_f16 v[40:43], v[136:139], v[180:183], v[40:43]
	v_mfma_f32_16x16x32_f16 v[32:35], v[128:131], v[188:191], v[32:35]
	v_mfma_f32_16x16x32_f16 v[24:27], v[136:139], v[188:191], v[24:27]
	v_mfma_f32_16x16x32_f16 v[16:19], v[128:131], v[196:199], v[16:19]
	v_mfma_f32_16x16x32_f16 v[8:11], v[136:139], v[196:199], v[8:11]
	v_mfma_f32_16x16x32_f16 v[60:63], v[132:135], v[176:179], v[60:63]
	v_mfma_f32_16x16x32_f16 v[56:59], v[140:143], v[176:179], v[56:59]
	v_mfma_f32_16x16x32_f16 v[48:51], v[132:135], v[184:187], v[48:51]
	v_mfma_f32_16x16x32_f16 v[40:43], v[140:143], v[184:187], v[40:43]
	v_mfma_f32_16x16x32_f16 v[32:35], v[132:135], v[192:195], v[32:35]
	v_mfma_f32_16x16x32_f16 v[24:27], v[140:143], v[192:195], v[24:27]
	v_mfma_f32_16x16x32_f16 v[16:19], v[132:135], v[200:203], v[16:19]
	v_mfma_f32_16x16x32_f16 v[8:11], v[140:143], v[200:203], v[8:11]
	s_setprio 0
	s_barrier
	s_add_u32 s74, s30, 0xc000
	s_addc_u32 s75, s31, 0
	s_add_i32 s76, s66, s42
	v_lshl_add_u64 v[128:129], s[74:75], 0, v[146:147]
	s_mov_b32 m0, s76
	s_nop 0
	global_load_lds_dwordx4 v[128:129], off
	v_lshl_add_u64 v[128:129], s[74:75], 0, v[150:151]
	s_add_i32 m0, s76, 0x2000
	s_nop 0
	global_load_lds_dwordx4 v[128:129], off
	s_waitcnt vmcnt(6)
	s_barrier
	s_setprio 1
	v_mfma_f32_16x16x32_f16 v[52:55], v[204:207], v[158:161], v[52:55]
	v_mfma_f32_16x16x32_f16 v[44:47], v[212:215], v[158:161], v[44:47]
	v_mfma_f32_16x16x32_f16 v[36:39], v[204:207], v[180:183], v[36:39]
	v_mfma_f32_16x16x32_f16 v[28:31], v[212:215], v[180:183], v[28:31]
	v_mfma_f32_16x16x32_f16 v[20:23], v[204:207], v[188:191], v[20:23]
	v_mfma_f32_16x16x32_f16 v[12:15], v[212:215], v[188:191], v[12:15]
	v_mfma_f32_16x16x32_f16 v[4:7], v[204:207], v[196:199], v[4:7]
	v_mfma_f32_16x16x32_f16 v[0:3], v[212:215], v[196:199], v[0:3]
	v_mfma_f32_16x16x32_f16 v[52:55], v[208:211], v[176:179], v[52:55]
	v_mfma_f32_16x16x32_f16 v[44:47], v[216:219], v[176:179], v[44:47]
	v_mfma_f32_16x16x32_f16 v[36:39], v[208:211], v[184:187], v[36:39]
	v_mfma_f32_16x16x32_f16 v[28:31], v[216:219], v[184:187], v[28:31]
	v_mfma_f32_16x16x32_f16 v[20:23], v[208:211], v[192:195], v[20:23]
	v_mfma_f32_16x16x32_f16 v[12:15], v[216:219], v[192:195], v[12:15]
	v_mfma_f32_16x16x32_f16 v[4:7], v[208:211], v[200:203], v[4:7]
	v_mfma_f32_16x16x32_f16 v[0:3], v[216:219], v[200:203], v[0:3]
	s_setprio 0
	s_add_i32 s74, 0, 0x18000
	v_add_u32_e32 v140, s74, v166
	s_barrier
	ds_read_b128 v[128:131], v140
	ds_read_b128 v[132:135], v140 offset:1024
	ds_read_b128 v[136:139], v140 offset:2048
	ds_read_b128 v[140:143], v140 offset:3072
	s_add_u32 s34, s34, 0x30000
	s_addc_u32 s35, s35, 0
	s_mov_b32 m0, s45
	v_lshl_add_u64 v[204:205], s[34:35], 0, v[144:145]
	ds_read_b128 v[158:161], v171 offset:32768
	ds_read_b128 v[176:179], v171 offset:33792
	ds_read_b128 v[180:183], v171 offset:34816
	ds_read_b128 v[184:187], v171 offset:35840
	ds_read_b128 v[188:191], v171 offset:36864
	ds_read_b128 v[192:195], v171 offset:37888
	ds_read_b128 v[196:199], v171 offset:38912
	ds_read_b128 v[200:203], v171 offset:39936
	global_load_lds_dwordx4 v[204:205], off
	v_lshl_add_u64 v[204:205], s[34:35], 0, v[148:149]
	s_mov_b32 m0, s46
	s_nop 0
	global_load_lds_dwordx4 v[204:205], off
	s_waitcnt lgkmcnt(8)
	s_barrier
	s_waitcnt lgkmcnt(0)
	s_setprio 1
	s_waitcnt lgkmcnt(0)
	v_mfma_f32_16x16x32_f16 v[124:127], v[128:131], v[158:161], v[124:127]
	v_mfma_f32_16x16x32_f16 v[120:123], v[136:139], v[158:161], v[120:123]
	v_mfma_f32_16x16x32_f16 v[108:111], v[128:131], v[180:183], v[108:111]
	v_mfma_f32_16x16x32_f16 v[104:107], v[136:139], v[180:183], v[104:107]
	v_mfma_f32_16x16x32_f16 v[96:99], v[128:131], v[188:191], v[96:99]
	v_mfma_f32_16x16x32_f16 v[88:91], v[136:139], v[188:191], v[88:91]
	v_mfma_f32_16x16x32_f16 v[80:83], v[128:131], v[196:199], v[80:83]
	v_mfma_f32_16x16x32_f16 v[72:75], v[136:139], v[196:199], v[72:75]
	v_mfma_f32_16x16x32_f16 v[124:127], v[132:135], v[176:179], v[124:127]
	v_mfma_f32_16x16x32_f16 v[120:123], v[140:143], v[176:179], v[120:123]
	v_mfma_f32_16x16x32_f16 v[108:111], v[132:135], v[184:187], v[108:111]
	v_mfma_f32_16x16x32_f16 v[104:107], v[140:143], v[184:187], v[104:107]
	v_mfma_f32_16x16x32_f16 v[96:99], v[132:135], v[192:195], v[96:99]
	v_mfma_f32_16x16x32_f16 v[88:91], v[140:143], v[192:195], v[88:91]
	v_mfma_f32_16x16x32_f16 v[80:83], v[132:135], v[200:203], v[80:83]
	v_mfma_f32_16x16x32_f16 v[72:75], v[140:143], v[200:203], v[72:75]
	s_setprio 0
	s_barrier
	s_add_i32 s34, 0, 0x1c000
	s_add_i32 s35, s74, s42
	v_add_u32_e32 v175, s34, v166
	v_lshl_add_u64 v[162:163], v[162:163], 0, s[26:27]
	s_mov_b32 m0, s35
	ds_read_b128 v[204:207], v175
	ds_read_b128 v[208:211], v175 offset:1024
	ds_read_b128 v[212:215], v175 offset:2048
	ds_read_b128 v[216:219], v175 offset:3072
	global_load_lds_dwordx4 v[162:163], off
	v_lshl_add_u64 v[162:163], v[220:221], 0, s[26:27]
	s_add_i32 m0, s35, 0x2000
	s_nop 0
	global_load_lds_dwordx4 v[162:163], off
	s_barrier
	s_waitcnt lgkmcnt(0)
	s_setprio 1
	s_waitcnt lgkmcnt(0)
	v_mfma_f32_16x16x32_f16 v[116:119], v[204:207], v[158:161], v[116:119]
	v_mfma_f32_16x16x32_f16 v[112:115], v[212:215], v[158:161], v[112:115]
	v_mfma_f32_16x16x32_f16 v[100:103], v[204:207], v[180:183], v[100:103]
	v_mfma_f32_16x16x32_f16 v[92:95], v[212:215], v[180:183], v[92:95]
	v_mfma_f32_16x16x32_f16 v[84:87], v[204:207], v[188:191], v[84:87]
	v_mfma_f32_16x16x32_f16 v[76:79], v[212:215], v[188:191], v[76:79]
	v_mfma_f32_16x16x32_f16 v[68:71], v[204:207], v[196:199], v[68:71]
	v_mfma_f32_16x16x32_f16 v[64:67], v[212:215], v[196:199], v[64:67]
	v_mfma_f32_16x16x32_f16 v[116:119], v[208:211], v[176:179], v[116:119]
	v_mfma_f32_16x16x32_f16 v[112:115], v[216:219], v[176:179], v[112:115]
	v_mfma_f32_16x16x32_f16 v[100:103], v[208:211], v[184:187], v[100:103]
	v_mfma_f32_16x16x32_f16 v[92:95], v[216:219], v[184:187], v[92:95]
	v_mfma_f32_16x16x32_f16 v[84:87], v[208:211], v[192:195], v[84:87]
	v_mfma_f32_16x16x32_f16 v[76:79], v[216:219], v[192:195], v[76:79]
	v_mfma_f32_16x16x32_f16 v[68:71], v[208:211], v[200:203], v[68:71]
	v_mfma_f32_16x16x32_f16 v[64:67], v[216:219], v[200:203], v[64:67]
	s_setprio 0
	s_mov_b32 m0, s49
	v_lshl_add_u64 v[162:163], v[222:223], 0, s[26:27]
	s_barrier
	ds_read_b128 v[158:161], v171 offset:49152
	ds_read_b128 v[176:179], v171 offset:50176
	ds_read_b128 v[180:183], v171 offset:51200
	ds_read_b128 v[184:187], v171 offset:52224
	ds_read_b128 v[188:191], v171 offset:53248
	ds_read_b128 v[192:195], v171 offset:54272
	ds_read_b128 v[196:199], v171 offset:55296
	ds_read_b128 v[200:203], v171 offset:56320
	global_load_lds_dwordx4 v[162:163], off
	v_lshl_add_u64 v[162:163], v[224:225], 0, s[26:27]
	s_mov_b32 m0, s50
	s_nop 0
	global_load_lds_dwordx4 v[162:163], off
	s_barrier
	s_waitcnt lgkmcnt(0)
	s_setprio 1
	s_waitcnt lgkmcnt(0)
	v_mfma_f32_16x16x32_f16 v[60:63], v[128:131], v[158:161], v[60:63]
	v_mfma_f32_16x16x32_f16 v[56:59], v[136:139], v[158:161], v[56:59]
	v_mfma_f32_16x16x32_f16 v[48:51], v[128:131], v[180:183], v[48:51]
	v_mfma_f32_16x16x32_f16 v[40:43], v[136:139], v[180:183], v[40:43]
	v_mfma_f32_16x16x32_f16 v[32:35], v[128:131], v[188:191], v[32:35]
	v_mfma_f32_16x16x32_f16 v[24:27], v[136:139], v[188:191], v[24:27]
	v_mfma_f32_16x16x32_f16 v[16:19], v[128:131], v[196:199], v[16:19]
	v_mfma_f32_16x16x32_f16 v[8:11], v[136:139], v[196:199], v[8:11]
	v_mfma_f32_16x16x32_f16 v[60:63], v[132:135], v[176:179], v[60:63]
	v_mfma_f32_16x16x32_f16 v[56:59], v[140:143], v[176:179], v[56:59]
	v_mfma_f32_16x16x32_f16 v[48:51], v[132:135], v[184:187], v[48:51]
	v_mfma_f32_16x16x32_f16 v[40:43], v[140:143], v[184:187], v[40:43]
	v_mfma_f32_16x16x32_f16 v[32:35], v[132:135], v[192:195], v[32:35]
	v_mfma_f32_16x16x32_f16 v[24:27], v[140:143], v[192:195], v[24:27]
	v_mfma_f32_16x16x32_f16 v[16:19], v[132:135], v[200:203], v[16:19]
	v_mfma_f32_16x16x32_f16 v[8:11], v[140:143], v[200:203], v[8:11]
	s_setprio 0
	s_barrier
	s_add_u32 s30, s30, 0xc080
	s_addc_u32 s31, s31, 0
	s_add_i32 s34, s34, s42
	v_lshl_add_u64 v[128:129], s[30:31], 0, v[146:147]
	s_mov_b32 m0, s34
	s_nop 0
	global_load_lds_dwordx4 v[128:129], off
	v_lshl_add_u64 v[128:129], s[30:31], 0, v[150:151]
	s_add_i32 m0, s34, 0x2000
	s_nop 0
	global_load_lds_dwordx4 v[128:129], off
	s_waitcnt vmcnt(6)
	s_barrier
	s_setprio 1
	v_mfma_f32_16x16x32_f16 v[52:55], v[204:207], v[158:161], v[52:55]
	v_mfma_f32_16x16x32_f16 v[44:47], v[212:215], v[158:161], v[44:47]
	v_mfma_f32_16x16x32_f16 v[36:39], v[204:207], v[180:183], v[36:39]
	v_mfma_f32_16x16x32_f16 v[28:31], v[212:215], v[180:183], v[28:31]
	v_mfma_f32_16x16x32_f16 v[20:23], v[204:207], v[188:191], v[20:23]
	v_mfma_f32_16x16x32_f16 v[12:15], v[212:215], v[188:191], v[12:15]
	v_mfma_f32_16x16x32_f16 v[4:7], v[204:207], v[196:199], v[4:7]
	v_mfma_f32_16x16x32_f16 v[0:3], v[212:215], v[196:199], v[0:3]
	v_mfma_f32_16x16x32_f16 v[52:55], v[208:211], v[176:179], v[52:55]
	v_mfma_f32_16x16x32_f16 v[44:47], v[216:219], v[176:179], v[44:47]
	v_mfma_f32_16x16x32_f16 v[36:39], v[208:211], v[184:187], v[36:39]
	v_mfma_f32_16x16x32_f16 v[28:31], v[216:219], v[184:187], v[28:31]
	v_mfma_f32_16x16x32_f16 v[20:23], v[208:211], v[192:195], v[20:23]
	v_mfma_f32_16x16x32_f16 v[12:15], v[216:219], v[192:195], v[12:15]
	v_mfma_f32_16x16x32_f16 v[4:7], v[208:211], v[200:203], v[4:7]
	v_mfma_f32_16x16x32_f16 v[0:3], v[216:219], v[200:203], v[0:3]
	s_setprio 0
	s_add_i32 s73, s73, 2
	s_add_u32 s28, s28, 0x100
	s_addc_u32 s29, s29, 0
	s_add_u32 s71, s71, 0x100
	s_addc_u32 s72, s72, 0
	s_cmp_gt_u32 s73, 9
	s_barrier
	s_cbranch_scc0 .LBB7_27
	s_lshl_b32 s28, s70, 8
	s_add_i32 s28, s28, s48
	s_lshl_b32 s29, s67, 8
	s_or_b32 s29, s29, s51
	s_waitcnt vmcnt(6)
	v_pk_fma_f32 v[126:127], v[126:127], v[226:227], v[236:237] op_sel_hi:[1,0,1]
	v_pk_fma_f32 v[124:125], v[124:125], v[226:227], v[234:235] op_sel_hi:[1,0,1]
	v_pk_fma_f32 v[186:187], v[122:123], v[226:227], v[240:241] op_sel_hi:[1,0,1]
	v_pk_fma_f32 v[122:123], v[120:121], v[226:227], v[238:239] op_sel_hi:[1,0,1]
	v_cvt_pk_f16_f32 v120, v124, v125
	v_cvt_pk_f16_f32 v121, v126, v127
	v_cvt_pk_f16_f32 v122, v122, v123
	v_cvt_pk_f16_f32 v123, v186, v187
	ds_write_b128 v173, v[120:123]
	v_pk_fma_f32 v[118:119], v[118:119], v[226:227], v[244:245] op_sel_hi:[1,0,1]
	v_pk_fma_f32 v[116:117], v[116:117], v[226:227], v[242:243] op_sel_hi:[1,0,1]
	v_pk_fma_f32 v[120:121], v[114:115], v[226:227], v[248:249] op_sel_hi:[1,0,1]
	v_pk_fma_f32 v[114:115], v[112:113], v[226:227], v[246:247] op_sel_hi:[1,0,1]
	v_cvt_pk_f16_f32 v112, v116, v117
	v_cvt_pk_f16_f32 v113, v118, v119
	v_cvt_pk_f16_f32 v114, v114, v115
	v_cvt_pk_f16_f32 v115, v120, v121
	ds_write_b128 v173, v[112:115] offset:64
	v_or_b32_e32 v116, s28, v167
	ds_read_b128 v[112:115], v174
	v_mul_lo_u32 v116, v116, s10
	v_add_u32_e32 v120, s29, v116
	v_lshlrev_b32_e32 v121, 1, v120
	v_add_u32_e32 v122, v121, v168
	ds_read_b128 v[116:119], v174 offset:1152
	s_waitcnt lgkmcnt(0)
	buffer_store_dwordx4 v[112:115], v122, s[20:23], 0 offen nt
	v_pk_fma_f32 v[110:111], v[110:111], v[226:227], v[236:237] op_sel:[0,1,0]
	v_pk_fma_f32 v[108:109], v[108:109], v[226:227], v[234:235] op_sel:[0,1,0]
	v_pk_fma_f32 v[112:113], v[106:107], v[226:227], v[240:241] op_sel:[0,1,0]
	v_pk_fma_f32 v[106:107], v[104:105], v[226:227], v[238:239] op_sel:[0,1,0]
	v_cvt_pk_f16_f32 v104, v108, v109
	v_cvt_pk_f16_f32 v105, v110, v111
	v_cvt_pk_f16_f32 v106, v106, v107
	v_cvt_pk_f16_f32 v107, v112, v113
	ds_write_b128 v173, v[104:107]
	v_pk_fma_f32 v[102:103], v[102:103], v[226:227], v[244:245] op_sel:[0,1,0]
	v_pk_fma_f32 v[100:101], v[100:101], v[226:227], v[242:243] op_sel:[0,1,0]
	v_pk_fma_f32 v[104:105], v[94:95], v[226:227], v[248:249] op_sel:[0,1,0]
	v_pk_fma_f32 v[94:95], v[92:93], v[226:227], v[246:247] op_sel:[0,1,0]
	v_cvt_pk_f16_f32 v92, v100, v101
	v_cvt_pk_f16_f32 v93, v102, v103
	v_cvt_pk_f16_f32 v94, v94, v95
	v_cvt_pk_f16_f32 v95, v104, v105
	ds_write_b128 v173, v[92:95] offset:64
	ds_read_b128 v[92:95], v174
	ds_read_b128 v[100:103], v174 offset:1152
	v_add_u32_e32 v104, s55, v121
	v_add_u32_e32 v114, v121, v169
	v_add_u32_e32 v105, v104, v168
	buffer_store_dwordx4 v[116:119], v114, s[20:23], 0 offen nt
	s_waitcnt lgkmcnt(1)
	buffer_store_dwordx4 v[92:95], v105, s[20:23], 0 offen nt
	v_pk_fma_f32 v[86:87], v[86:87], v[228:229], v[244:245] op_sel_hi:[1,0,1]
	v_pk_fma_f32 v[84:85], v[84:85], v[228:229], v[242:243] op_sel_hi:[1,0,1]
	v_pk_fma_f32 v[92:93], v[98:99], v[228:229], v[236:237] op_sel_hi:[1,0,1]
	v_pk_fma_f32 v[94:95], v[96:97], v[228:229], v[234:235] op_sel_hi:[1,0,1]
	v_pk_fma_f32 v[96:97], v[90:91], v[228:229], v[240:241] op_sel_hi:[1,0,1]
	v_pk_fma_f32 v[90:91], v[88:89], v[228:229], v[238:239] op_sel_hi:[1,0,1]
	v_cvt_pk_f16_f32 v88, v94, v95
	v_cvt_pk_f16_f32 v89, v92, v93
	v_cvt_pk_f16_f32 v90, v90, v91
	v_cvt_pk_f16_f32 v91, v96, v97
	ds_write_b128 v173, v[88:91]
	v_pk_fma_f32 v[88:89], v[78:79], v[228:229], v[248:249] op_sel_hi:[1,0,1]
	v_pk_fma_f32 v[78:79], v[76:77], v[228:229], v[246:247] op_sel_hi:[1,0,1]
	v_cvt_pk_f16_f32 v76, v84, v85
	v_cvt_pk_f16_f32 v77, v86, v87
	v_cvt_pk_f16_f32 v78, v78, v79
	v_cvt_pk_f16_f32 v79, v88, v89
	ds_write_b128 v173, v[76:79] offset:64
	ds_read_b128 v[76:79], v174
	ds_read_b128 v[84:87], v174 offset:1152
	v_add_u32_e32 v88, s55, v104
	v_add_u32_e32 v105, v104, v169
	v_add_u32_e32 v89, v88, v168
	s_waitcnt lgkmcnt(4)
	buffer_store_dwordx4 v[100:103], v105, s[20:23], 0 offen nt
	s_waitcnt lgkmcnt(1)
	buffer_store_dwordx4 v[76:79], v89, s[20:23], 0 offen nt
	v_pk_fma_f32 v[70:71], v[70:71], v[228:229], v[244:245] op_sel:[0,1,0]
	v_pk_fma_f32 v[68:69], v[68:69], v[228:229], v[242:243] op_sel:[0,1,0]
	v_add_u32_e32 v76, v88, v169
	s_waitcnt lgkmcnt(0)
	buffer_store_dwordx4 v[84:87], v76, s[20:23], 0 offen nt
	v_pk_fma_f32 v[76:77], v[82:83], v[228:229], v[236:237] op_sel:[0,1,0]
	v_pk_fma_f32 v[78:79], v[80:81], v[228:229], v[234:235] op_sel:[0,1,0]
	v_pk_fma_f32 v[80:81], v[74:75], v[228:229], v[240:241] op_sel:[0,1,0]
	v_pk_fma_f32 v[74:75], v[72:73], v[228:229], v[238:239] op_sel:[0,1,0]
	v_cvt_pk_f16_f32 v72, v78, v79
	v_cvt_pk_f16_f32 v73, v76, v77
	v_cvt_pk_f16_f32 v74, v74, v75
	v_cvt_pk_f16_f32 v75, v80, v81
	ds_write_b128 v173, v[72:75]
	v_pk_fma_f32 v[72:73], v[66:67], v[228:229], v[248:249] op_sel:[0,1,0]
	v_pk_fma_f32 v[66:67], v[64:65], v[228:229], v[246:247] op_sel:[0,1,0]
	v_cvt_pk_f16_f32 v64, v68, v69
	v_cvt_pk_f16_f32 v65, v70, v71
	v_cvt_pk_f16_f32 v66, v66, v67
	v_cvt_pk_f16_f32 v67, v72, v73
	ds_write_b128 v173, v[64:67] offset:64
	ds_read_b128 v[64:67], v174
	ds_read_b128 v[68:71], v174 offset:1152
	v_add_u32_e32 v72, s56, v120
	v_lshlrev_b32_e32 v73, 1, v72
	v_add_u32_e32 v74, v73, v168
	s_waitcnt lgkmcnt(1)
	buffer_store_dwordx4 v[64:67], v74, s[20:23], 0 offen nt
	v_pk_fma_f32 v[62:63], v[62:63], v[230:231], v[236:237] op_sel_hi:[1,0,1]
	v_pk_fma_f32 v[60:61], v[60:61], v[230:231], v[234:235] op_sel_hi:[1,0,1]
	v_pk_fma_f32 v[64:65], v[58:59], v[230:231], v[240:241] op_sel_hi:[1,0,1]
	v_pk_fma_f32 v[58:59], v[56:57], v[230:231], v[238:239] op_sel_hi:[1,0,1]
	v_cvt_pk_f16_f32 v56, v60, v61
	v_cvt_pk_f16_f32 v57, v62, v63
	v_cvt_pk_f16_f32 v58, v58, v59
	v_cvt_pk_f16_f32 v59, v64, v65
	ds_write_b128 v173, v[56:59]
	v_pk_fma_f32 v[54:55], v[54:55], v[230:231], v[244:245] op_sel_hi:[1,0,1]
	v_pk_fma_f32 v[52:53], v[52:53], v[230:231], v[242:243] op_sel_hi:[1,0,1]
	v_pk_fma_f32 v[56:57], v[46:47], v[230:231], v[248:249] op_sel_hi:[1,0,1]
	v_pk_fma_f32 v[46:47], v[44:45], v[230:231], v[246:247] op_sel_hi:[1,0,1]
	v_cvt_pk_f16_f32 v44, v52, v53
	v_cvt_pk_f16_f32 v45, v54, v55
	v_cvt_pk_f16_f32 v46, v46, v47
	v_cvt_pk_f16_f32 v47, v56, v57
	ds_write_b128 v173, v[44:47] offset:64
	ds_read_b128 v[44:47], v174
	ds_read_b128 v[52:55], v174 offset:1152
	v_add_u32_e32 v56, s62, v88
	v_add_u32_e32 v66, v73, v169
	v_add_u32_e32 v57, v56, v168
	s_waitcnt lgkmcnt(4)
	buffer_store_dwordx4 v[68:71], v66, s[20:23], 0 offen nt
	s_waitcnt lgkmcnt(1)
	buffer_store_dwordx4 v[44:47], v57, s[20:23], 0 offen nt
	v_pk_fma_f32 v[38:39], v[38:39], v[230:231], v[244:245] op_sel:[0,1,0]
	v_pk_fma_f32 v[36:37], v[36:37], v[230:231], v[242:243] op_sel:[0,1,0]
	v_add_u32_e32 v44, v56, v169
	s_waitcnt lgkmcnt(0)
	buffer_store_dwordx4 v[52:55], v44, s[20:23], 0 offen nt
	v_pk_fma_f32 v[44:45], v[50:51], v[230:231], v[236:237] op_sel:[0,1,0]
	v_pk_fma_f32 v[46:47], v[48:49], v[230:231], v[234:235] op_sel:[0,1,0]
	v_pk_fma_f32 v[48:49], v[42:43], v[230:231], v[240:241] op_sel:[0,1,0]
	v_pk_fma_f32 v[42:43], v[40:41], v[230:231], v[238:239] op_sel:[0,1,0]
	v_cvt_pk_f16_f32 v40, v46, v47
	v_cvt_pk_f16_f32 v41, v44, v45
	v_cvt_pk_f16_f32 v42, v42, v43
	v_cvt_pk_f16_f32 v43, v48, v49
	ds_write_b128 v173, v[40:43]
	v_pk_fma_f32 v[40:41], v[30:31], v[230:231], v[248:249] op_sel:[0,1,0]
	v_pk_fma_f32 v[30:31], v[28:29], v[230:231], v[246:247] op_sel:[0,1,0]
	v_cvt_pk_f16_f32 v28, v36, v37
	v_cvt_pk_f16_f32 v29, v38, v39
	v_cvt_pk_f16_f32 v30, v30, v31
	v_cvt_pk_f16_f32 v31, v40, v41
	ds_write_b128 v173, v[28:31] offset:64
	ds_read_b128 v[28:31], v174
	ds_read_b128 v[36:39], v174 offset:1152
	v_add_u32_e32 v40, s63, v72
	v_lshlrev_b32_e32 v41, 1, v40
	v_add_u32_e32 v42, v41, v168
	s_waitcnt lgkmcnt(1)
	buffer_store_dwordx4 v[28:31], v42, s[20:23], 0 offen nt
	v_pk_fma_f32 v[22:23], v[22:23], v[232:233], v[244:245] op_sel_hi:[1,0,1]
	v_pk_fma_f32 v[20:21], v[20:21], v[232:233], v[242:243] op_sel_hi:[1,0,1]
	v_add_u32_e32 v28, v41, v169
	s_waitcnt lgkmcnt(0)
	buffer_store_dwordx4 v[36:39], v28, s[20:23], 0 offen nt
	v_pk_fma_f32 v[28:29], v[34:35], v[232:233], v[236:237] op_sel_hi:[1,0,1]
	v_pk_fma_f32 v[30:31], v[32:33], v[232:233], v[234:235] op_sel_hi:[1,0,1]
	v_pk_fma_f32 v[32:33], v[26:27], v[232:233], v[240:241] op_sel_hi:[1,0,1]
	v_pk_fma_f32 v[26:27], v[24:25], v[232:233], v[238:239] op_sel_hi:[1,0,1]
	v_cvt_pk_f16_f32 v24, v30, v31
	v_cvt_pk_f16_f32 v25, v28, v29
	v_cvt_pk_f16_f32 v26, v26, v27
	v_cvt_pk_f16_f32 v27, v32, v33
	ds_write_b128 v173, v[24:27]
	v_pk_fma_f32 v[24:25], v[14:15], v[232:233], v[248:249] op_sel_hi:[1,0,1]
	v_pk_fma_f32 v[14:15], v[12:13], v[232:233], v[246:247] op_sel_hi:[1,0,1]
	v_cvt_pk_f16_f32 v12, v20, v21
	v_cvt_pk_f16_f32 v13, v22, v23
	v_cvt_pk_f16_f32 v14, v14, v15
	v_cvt_pk_f16_f32 v15, v24, v25
	ds_write_b128 v173, v[12:15] offset:64
	ds_read_b128 v[12:15], v174
	ds_read_b128 v[20:23], v174 offset:1152
	v_add_u32_e32 v24, s64, v40
	v_lshlrev_b32_e32 v25, 1, v24
	v_add_u32_e32 v26, v25, v168
	s_waitcnt lgkmcnt(1)
	buffer_store_dwordx4 v[12:15], v26, s[20:23], 0 offen nt
	v_pk_fma_f32 v[6:7], v[6:7], v[232:233], v[244:245] op_sel:[0,1,0]
	v_pk_fma_f32 v[4:5], v[4:5], v[232:233], v[242:243] op_sel:[0,1,0]
	v_pk_fma_f32 v[12:13], v[18:19], v[232:233], v[236:237] op_sel:[0,1,0]
	v_pk_fma_f32 v[14:15], v[16:17], v[232:233], v[234:235] op_sel:[0,1,0]
	v_pk_fma_f32 v[16:17], v[10:11], v[232:233], v[240:241] op_sel:[0,1,0]
	v_pk_fma_f32 v[10:11], v[8:9], v[232:233], v[238:239] op_sel:[0,1,0]
	v_cvt_pk_f16_f32 v8, v14, v15
	v_cvt_pk_f16_f32 v9, v12, v13
	v_cvt_pk_f16_f32 v10, v10, v11
	v_cvt_pk_f16_f32 v11, v16, v17
	ds_write_b128 v173, v[8:11]
	v_pk_fma_f32 v[8:9], v[2:3], v[232:233], v[248:249] op_sel:[0,1,0]
	v_pk_fma_f32 v[2:3], v[0:1], v[232:233], v[246:247] op_sel:[0,1,0]
	v_cvt_pk_f16_f32 v0, v4, v5
	v_cvt_pk_f16_f32 v1, v6, v7
	v_cvt_pk_f16_f32 v2, v2, v3
	v_cvt_pk_f16_f32 v3, v8, v9
	ds_write_b128 v173, v[0:3] offset:64
	ds_read_b128 v[0:3], v174
	ds_read_b128 v[4:7], v174 offset:1152
	v_add_lshl_u32 v8, v24, s64, 1
	v_add_u32_e32 v25, v25, v169
	v_add_u32_e32 v9, v8, v168
	s_waitcnt lgkmcnt(4)
	buffer_store_dwordx4 v[20:23], v25, s[20:23], 0 offen nt
	s_waitcnt lgkmcnt(1)
	buffer_store_dwordx4 v[0:3], v9, s[20:23], 0 offen nt
	s_mov_b32 s67, s68
	s_mov_b32 s70, s69
	v_add_u32_e32 v0, v8, v169
	s_mov_b64 s[30:31], s[0:1]
	s_mov_b64 s[28:29], s[8:9]
	s_mov_b64 vcc, s[6:7]
	s_waitcnt lgkmcnt(0)
	buffer_store_dwordx4 v[4:7], v0, s[20:23], 0 offen nt
	s_cbranch_vccz .LBB7_12
	s_waitcnt vmcnt(0)
	s_cmpk_gt_u32 s36, 0xff
	s_cbranch_scc1 .LBB7_31
	s_barrier

.LBB7_32:
	s_endpgm
	s_endpgm
	s_endpgm
	s_endpgm
	s_endpgm
	s_endpgm
	s_endpgm
	s_endpgm
	s_endpgm
	s_endpgm
	s_endpgm
	s_endpgm
	s_endpgm
	s_endpgm
	s_endpgm
	s_endpgm
	s_endpgm
	s_endpgm
	s_endpgm
	s_endpgm
	s_endpgm
	s_endpgm
	s_endpgm
	s_endpgm
	s_endpgm
	s_endpgm
	s_endpgm
	s_endpgm
	s_endpgm
	s_endpgm
	s_endpgm
	s_endpgm
	s_endpgm
	s_endpgm
	s_endpgm
	s_endpgm
	s_endpgm
	s_endpgm
	s_endpgm
	s_endpgm
	s_endpgm
	s_endpgm
	s_endpgm
	s_endpgm
	s_endpgm
	s_endpgm
	s_endpgm
	s_endpgm
	s_endpgm
	s_endpgm
	s_endpgm
	s_endpgm
	s_endpgm
	s_endpgm
	s_endpgm

	.amdhsa_kernel _Z6k_gemmIN2pg6EpiLinILi0EEELi768EEvNS0_4GemmET_
		.amdhsa_group_segment_fixed_size 0
		.amdhsa_private_segment_fixed_size 0
		.amdhsa_kernarg_size 320
		.amdhsa_user_sgpr_count 2
		.amdhsa_user_sgpr_dispatch_ptr 0
		.amdhsa_user_sgpr_queue_ptr 0
		.amdhsa_user_sgpr_kernarg_segment_ptr 1
		.amdhsa_user_sgpr_dispatch_id 0
		.amdhsa_user_sgpr_kernarg_preload_length 0
		.amdhsa_user_sgpr_kernarg_preload_offset 0
		.amdhsa_user_sgpr_private_segment_size 0
		.amdhsa_uses_dynamic_stack 0
		.amdhsa_enable_private_segment 0
		.amdhsa_system_sgpr_workgroup_id_x 1
		.amdhsa_system_sgpr_workgroup_id_y 0
		.amdhsa_system_sgpr_workgroup_id_z 0
		.amdhsa_system_sgpr_workgroup_info 0
		.amdhsa_system_vgpr_workitem_id 0
		.amdhsa_next_free_vgpr 254
		.amdhsa_next_free_sgpr 77
		.amdhsa_accum_offset 256
		.amdhsa_reserve_vcc 1
		.amdhsa_float_round_mode_32 0
		.amdhsa_float_round_mode_16_64 0
		.amdhsa_float_denorm_mode_32 3
		.amdhsa_float_denorm_mode_16_64 3
		.amdhsa_dx10_clamp 1
		.amdhsa_ieee_mode 1
		.amdhsa_fp16_overflow 0
		.amdhsa_tg_split 0
		.amdhsa_exception_fp_ieee_invalid_op 0
		.amdhsa_exception_fp_denorm_src 0
		.amdhsa_exception_fp_ieee_div_zero 0
		.amdhsa_exception_fp_ieee_overflow 0
		.amdhsa_exception_fp_ieee_underflow 0
		.amdhsa_exception_fp_ieee_inexact 0
		.amdhsa_exception_int_div_zero 0
	.end_amdhsa_kernel

.LBB8_32:
	s_endpgm
	s_endpgm
	s_endpgm
	s_endpgm
	s_endpgm
	s_endpgm
	s_endpgm
	s_endpgm
	s_endpgm
	s_endpgm
	s_endpgm
	s_endpgm
	s_endpgm
	s_endpgm
	s_endpgm
	s_endpgm
	s_endpgm
	s_endpgm
	s_endpgm
	s_endpgm
	s_endpgm
	s_endpgm
	s_endpgm
	s_endpgm
	s_endpgm

.LBB9_26:
	s_lshl_b32 s34, s70, 8
	s_add_i32 s34, s34, s48
	v_or_b32_e32 v250, s34, v167
	v_ashrrev_i32_e32 v251, 31, v250
	v_lshl_add_u64 v[250:251], v[250:251], 3, s[12:13]
	s_lshl_b32 s35, s68, 8
	s_or_b32 s35, s35, s51
	v_or_b32_e32 v252, s35, v166
	v_ashrrev_i32_e32 v253, 31, v252
	v_lshl_add_u64 v[252:253], v[252:253], 2, s[14:15]
	global_load_dword v226, v[250:251], off offset:4
	global_load_dword v227, v[250:251], off offset:132
	global_load_dword v228, v[250:251], off offset:260
	global_load_dword v229, v[250:251], off offset:388
	global_load_dword v230, v[250:251], off offset:1028
	global_load_dword v231, v[250:251], off offset:1156
	global_load_dword v232, v[250:251], off offset:1284
	global_load_dword v233, v[250:251], off offset:1412
	global_load_dwordx4 v[234:237], v[252:253], off
	global_load_dwordx4 v[238:241], v[252:253], off offset:16
	global_load_dwordx4 v[242:245], v[252:253], off offset:128
	global_load_dwordx4 v[246:249], v[252:253], off offset:144
	s_add_u32 s28, s28, 0x30080
	s_addc_u32 s29, s29, 0
	s_add_u32 s71, s30, 0x100
	v_mov_b32_e32 v0, 0
	s_addc_u32 s72, s31, 0
	s_mov_b32 s73, -2
	v_mov_b32_e32 v1, v0
	v_mov_b32_e32 v2, v0
	v_mov_b32_e32 v3, v0
	v_mov_b32_e32 v4, v0
	v_mov_b32_e32 v5, v0
	v_mov_b32_e32 v6, v0
	v_mov_b32_e32 v7, v0
	v_mov_b32_e32 v12, v0
	v_mov_b32_e32 v13, v0
	v_mov_b32_e32 v14, v0
	v_mov_b32_e32 v15, v0
	v_mov_b32_e32 v20, v0
	v_mov_b32_e32 v21, v0
	v_mov_b32_e32 v22, v0
	v_mov_b32_e32 v23, v0
	v_mov_b32_e32 v28, v0
	v_mov_b32_e32 v29, v0
	v_mov_b32_e32 v30, v0
	v_mov_b32_e32 v31, v0
	v_mov_b32_e32 v36, v0
	v_mov_b32_e32 v37, v0
	v_mov_b32_e32 v38, v0
	v_mov_b32_e32 v39, v0
	v_mov_b32_e32 v44, v0
	v_mov_b32_e32 v45, v0
	v_mov_b32_e32 v46, v0
	v_mov_b32_e32 v47, v0
	v_mov_b32_e32 v52, v0
	v_mov_b32_e32 v53, v0
	v_mov_b32_e32 v54, v0
	v_mov_b32_e32 v55, v0
	v_mov_b32_e32 v8, v0
	v_mov_b32_e32 v9, v0
	v_mov_b32_e32 v10, v0
	v_mov_b32_e32 v11, v0
	v_mov_b32_e32 v16, v0
	v_mov_b32_e32 v17, v0
	v_mov_b32_e32 v18, v0
	v_mov_b32_e32 v19, v0
	v_mov_b32_e32 v24, v0
	v_mov_b32_e32 v25, v0
	v_mov_b32_e32 v26, v0
	v_mov_b32_e32 v27, v0
	v_mov_b32_e32 v32, v0
	v_mov_b32_e32 v33, v0
	v_mov_b32_e32 v34, v0
	v_mov_b32_e32 v35, v0
	v_mov_b32_e32 v40, v0
	v_mov_b32_e32 v41, v0
	v_mov_b32_e32 v42, v0
	v_mov_b32_e32 v43, v0
	v_mov_b32_e32 v48, v0
	v_mov_b32_e32 v49, v0
	v_mov_b32_e32 v50, v0
	v_mov_b32_e32 v51, v0
	v_mov_b32_e32 v56, v0
	v_mov_b32_e32 v57, v0
	v_mov_b32_e32 v58, v0
	v_mov_b32_e32 v59, v0
	v_mov_b32_e32 v60, v0
	v_mov_b32_e32 v61, v0
	v_mov_b32_e32 v62, v0
	v_mov_b32_e32 v63, v0
	v_mov_b32_e32 v64, v0
	v_mov_b32_e32 v65, v0
	v_mov_b32_e32 v66, v0
	v_mov_b32_e32 v67, v0
	v_mov_b32_e32 v68, v0
	v_mov_b32_e32 v69, v0
	v_mov_b32_e32 v70, v0
	v_mov_b32_e32 v71, v0
	v_mov_b32_e32 v76, v0
	v_mov_b32_e32 v77, v0
	v_mov_b32_e32 v78, v0
	v_mov_b32_e32 v79, v0
	v_mov_b32_e32 v84, v0
	v_mov_b32_e32 v85, v0
	v_mov_b32_e32 v86, v0
	v_mov_b32_e32 v87, v0
	v_mov_b32_e32 v92, v0
	v_mov_b32_e32 v93, v0
	v_mov_b32_e32 v94, v0
	v_mov_b32_e32 v95, v0
	v_mov_b32_e32 v100, v0
	v_mov_b32_e32 v101, v0
	v_mov_b32_e32 v102, v0
	v_mov_b32_e32 v103, v0
	v_mov_b32_e32 v112, v0
	v_mov_b32_e32 v113, v0
	v_mov_b32_e32 v114, v0
	v_mov_b32_e32 v115, v0
	v_mov_b32_e32 v116, v0
	v_mov_b32_e32 v117, v0
	v_mov_b32_e32 v118, v0
	v_mov_b32_e32 v119, v0
	v_mov_b32_e32 v72, v0
	v_mov_b32_e32 v73, v0
	v_mov_b32_e32 v74, v0
	v_mov_b32_e32 v75, v0
	v_mov_b32_e32 v80, v0
	v_mov_b32_e32 v81, v0
	v_mov_b32_e32 v82, v0
	v_mov_b32_e32 v83, v0
	v_mov_b32_e32 v88, v0
	v_mov_b32_e32 v89, v0
	v_mov_b32_e32 v90, v0
	v_mov_b32_e32 v91, v0
	v_mov_b32_e32 v96, v0
	v_mov_b32_e32 v97, v0
	v_mov_b32_e32 v98, v0
	v_mov_b32_e32 v99, v0
	v_mov_b32_e32 v104, v0
	v_mov_b32_e32 v105, v0
	v_mov_b32_e32 v106, v0
	v_mov_b32_e32 v107, v0
	v_mov_b32_e32 v108, v0
	v_mov_b32_e32 v109, v0
	v_mov_b32_e32 v110, v0
	v_mov_b32_e32 v111, v0
	v_mov_b32_e32 v120, v0
	v_mov_b32_e32 v121, v0
	v_mov_b32_e32 v122, v0
	v_mov_b32_e32 v123, v0
	v_mov_b32_e32 v124, v0
	v_mov_b32_e32 v125, v0
	v_mov_b32_e32 v126, v0
	v_mov_b32_e32 v127, v0
.LBB9_27:
	ds_read_b128 v[128:131], v172
	ds_read_b128 v[132:135], v172 offset:1024
	ds_read_b128 v[136:139], v172 offset:2048
	ds_read_b128 v[140:143], v172 offset:3072
	s_add_u32 s30, s28, 0xfffd0080
	s_addc_u32 s31, s29, -1
	s_cmp_eq_u32 s73, 8
	s_cselect_b32 s35, s9, s31
	s_cselect_b32 s34, s8, s30
	s_cselect_b32 s31, s1, s72
	s_cselect_b32 s30, s0, s71
	v_lshl_add_u64 v[202:203], s[28:29], 0, v[152:153]
	s_add_i32 m0, s43, 0xc000
	ds_read_b128 v[158:161], v173
	ds_read_b128 v[162:165], v173 offset:1024
	ds_read_b128 v[178:181], v173 offset:2048
	ds_read_b128 v[182:185], v173 offset:3072
	ds_read_b128 v[186:189], v173 offset:4096
	ds_read_b128 v[190:193], v173 offset:5120
	ds_read_b128 v[194:197], v173 offset:6144
	ds_read_b128 v[198:201], v173 offset:7168
	global_load_lds_dwordx4 v[202:203], off
	v_lshl_add_u64 v[202:203], s[28:29], 0, v[154:155]
	s_add_i32 m0, s43, 0xe000
	s_nop 0
	global_load_lds_dwordx4 v[202:203], off
	s_waitcnt lgkmcnt(8)
	s_barrier
	s_waitcnt lgkmcnt(0)
	s_setprio 1
	s_waitcnt lgkmcnt(0)
	v_mfma_f32_16x16x32_f16 v[124:127], v[128:131], v[158:161], v[124:127]
	v_mfma_f32_16x16x32_f16 v[120:123], v[136:139], v[158:161], v[120:123]
	v_mfma_f32_16x16x32_f16 v[108:111], v[128:131], v[178:181], v[108:111]
	v_mfma_f32_16x16x32_f16 v[104:107], v[136:139], v[178:181], v[104:107]
	v_mfma_f32_16x16x32_f16 v[96:99], v[128:131], v[186:189], v[96:99]
	v_mfma_f32_16x16x32_f16 v[88:91], v[136:139], v[186:189], v[88:91]
	v_mfma_f32_16x16x32_f16 v[80:83], v[128:131], v[194:197], v[80:83]
	v_mfma_f32_16x16x32_f16 v[72:75], v[136:139], v[194:197], v[72:75]
	v_mfma_f32_16x16x32_f16 v[124:127], v[132:135], v[162:165], v[124:127]
	v_mfma_f32_16x16x32_f16 v[120:123], v[140:143], v[162:165], v[120:123]
	v_mfma_f32_16x16x32_f16 v[108:111], v[132:135], v[182:185], v[108:111]
	v_mfma_f32_16x16x32_f16 v[104:107], v[140:143], v[182:185], v[104:107]
	v_mfma_f32_16x16x32_f16 v[96:99], v[132:135], v[190:193], v[96:99]
	v_mfma_f32_16x16x32_f16 v[88:91], v[140:143], v[190:193], v[88:91]
	v_mfma_f32_16x16x32_f16 v[80:83], v[132:135], v[198:201], v[80:83]
	v_mfma_f32_16x16x32_f16 v[72:75], v[140:143], v[198:201], v[72:75]
	s_setprio 0
	s_barrier
	s_add_i32 s74, s65, s42
	v_lshl_add_u64 v[218:219], s[30:31], 0, v[146:147]
	s_mov_b32 m0, s74
	ds_read_b128 v[202:205], v174
	ds_read_b128 v[206:209], v174 offset:1024
	ds_read_b128 v[210:213], v174 offset:2048
	ds_read_b128 v[214:217], v174 offset:3072
	global_load_lds_dwordx4 v[218:219], off
	v_lshl_add_u64 v[220:221], s[30:31], 0, v[150:151]
	s_add_i32 m0, s74, 0x2000
	s_nop 0
	global_load_lds_dwordx4 v[220:221], off
	s_barrier
	s_waitcnt lgkmcnt(0)
	s_setprio 1
	s_waitcnt lgkmcnt(0)
	v_mfma_f32_16x16x32_f16 v[116:119], v[202:205], v[158:161], v[116:119]
	v_mfma_f32_16x16x32_f16 v[112:115], v[210:213], v[158:161], v[112:115]
	v_mfma_f32_16x16x32_f16 v[100:103], v[202:205], v[178:181], v[100:103]
	v_mfma_f32_16x16x32_f16 v[92:95], v[210:213], v[178:181], v[92:95]
	v_mfma_f32_16x16x32_f16 v[84:87], v[202:205], v[186:189], v[84:87]
	v_mfma_f32_16x16x32_f16 v[76:79], v[210:213], v[186:189], v[76:79]
	v_mfma_f32_16x16x32_f16 v[68:71], v[202:205], v[194:197], v[68:71]
	v_mfma_f32_16x16x32_f16 v[64:67], v[210:213], v[194:197], v[64:67]
	v_mfma_f32_16x16x32_f16 v[116:119], v[206:209], v[162:165], v[116:119]
	v_mfma_f32_16x16x32_f16 v[112:115], v[214:217], v[162:165], v[112:115]
	v_mfma_f32_16x16x32_f16 v[100:103], v[206:209], v[182:185], v[100:103]
	v_mfma_f32_16x16x32_f16 v[92:95], v[214:217], v[182:185], v[92:95]
	v_mfma_f32_16x16x32_f16 v[84:87], v[206:209], v[190:193], v[84:87]
	v_mfma_f32_16x16x32_f16 v[76:79], v[214:217], v[190:193], v[76:79]
	v_mfma_f32_16x16x32_f16 v[68:71], v[206:209], v[198:201], v[68:71]
	v_mfma_f32_16x16x32_f16 v[64:67], v[214:217], v[198:201], v[64:67]
	s_setprio 0
	s_mov_b32 m0, s43
	v_lshl_add_u64 v[222:223], s[34:35], 0, v[144:145]
	s_barrier
	ds_read_b128 v[158:161], v173 offset:16384
	ds_read_b128 v[162:165], v173 offset:17408
	ds_read_b128 v[178:181], v173 offset:18432
	ds_read_b128 v[182:185], v173 offset:19456
	ds_read_b128 v[186:189], v173 offset:20480
	ds_read_b128 v[190:193], v173 offset:21504
	ds_read_b128 v[194:197], v173 offset:22528
	ds_read_b128 v[198:201], v173 offset:23552
	global_load_lds_dwordx4 v[222:223], off
	v_lshl_add_u64 v[224:225], s[34:35], 0, v[148:149]
	s_mov_b32 m0, s44
	s_nop 0
	global_load_lds_dwordx4 v[224:225], off
	s_barrier
	s_waitcnt lgkmcnt(0)
	s_setprio 1
	s_waitcnt lgkmcnt(0)
	v_mfma_f32_16x16x32_f16 v[60:63], v[128:131], v[158:161], v[60:63]
	v_mfma_f32_16x16x32_f16 v[56:59], v[136:139], v[158:161], v[56:59]
	v_mfma_f32_16x16x32_f16 v[48:51], v[128:131], v[178:181], v[48:51]
	v_mfma_f32_16x16x32_f16 v[40:43], v[136:139], v[178:181], v[40:43]
	v_mfma_f32_16x16x32_f16 v[32:35], v[128:131], v[186:189], v[32:35]
	v_mfma_f32_16x16x32_f16 v[24:27], v[136:139], v[186:189], v[24:27]
	v_mfma_f32_16x16x32_f16 v[16:19], v[128:131], v[194:197], v[16:19]
	v_mfma_f32_16x16x32_f16 v[8:11], v[136:139], v[194:197], v[8:11]
	v_mfma_f32_16x16x32_f16 v[60:63], v[132:135], v[162:165], v[60:63]
	v_mfma_f32_16x16x32_f16 v[56:59], v[140:143], v[162:165], v[56:59]
	v_mfma_f32_16x16x32_f16 v[48:51], v[132:135], v[182:185], v[48:51]
	v_mfma_f32_16x16x32_f16 v[40:43], v[140:143], v[182:185], v[40:43]
	v_mfma_f32_16x16x32_f16 v[32:35], v[132:135], v[190:193], v[32:35]
	v_mfma_f32_16x16x32_f16 v[24:27], v[140:143], v[190:193], v[24:27]
	v_mfma_f32_16x16x32_f16 v[16:19], v[132:135], v[198:201], v[16:19]
	v_mfma_f32_16x16x32_f16 v[8:11], v[140:143], v[198:201], v[8:11]
	s_setprio 0
	s_barrier
	s_add_u32 s74, s30, 0xc000
	s_addc_u32 s75, s31, 0
	s_add_i32 s76, s66, s42
	v_lshl_add_u64 v[128:129], s[74:75], 0, v[146:147]
	s_mov_b32 m0, s76
	s_nop 0
	global_load_lds_dwordx4 v[128:129], off
	v_lshl_add_u64 v[128:129], s[74:75], 0, v[150:151]
	s_add_i32 m0, s76, 0x2000
	s_nop 0
	global_load_lds_dwordx4 v[128:129], off
	s_waitcnt vmcnt(6)
	s_barrier
	s_setprio 1
	v_mfma_f32_16x16x32_f16 v[52:55], v[202:205], v[158:161], v[52:55]
	v_mfma_f32_16x16x32_f16 v[44:47], v[210:213], v[158:161], v[44:47]
	v_mfma_f32_16x16x32_f16 v[36:39], v[202:205], v[178:181], v[36:39]
	v_mfma_f32_16x16x32_f16 v[28:31], v[210:213], v[178:181], v[28:31]
	v_mfma_f32_16x16x32_f16 v[20:23], v[202:205], v[186:189], v[20:23]
	v_mfma_f32_16x16x32_f16 v[12:15], v[210:213], v[186:189], v[12:15]
	v_mfma_f32_16x16x32_f16 v[4:7], v[202:205], v[194:197], v[4:7]
	v_mfma_f32_16x16x32_f16 v[0:3], v[210:213], v[194:197], v[0:3]
	v_mfma_f32_16x16x32_f16 v[52:55], v[206:209], v[162:165], v[52:55]
	v_mfma_f32_16x16x32_f16 v[44:47], v[214:217], v[162:165], v[44:47]
	v_mfma_f32_16x16x32_f16 v[36:39], v[206:209], v[182:185], v[36:39]
	v_mfma_f32_16x16x32_f16 v[28:31], v[214:217], v[182:185], v[28:31]
	v_mfma_f32_16x16x32_f16 v[20:23], v[206:209], v[190:193], v[20:23]
	v_mfma_f32_16x16x32_f16 v[12:15], v[214:217], v[190:193], v[12:15]
	v_mfma_f32_16x16x32_f16 v[4:7], v[206:209], v[198:201], v[4:7]
	v_mfma_f32_16x16x32_f16 v[0:3], v[214:217], v[198:201], v[0:3]
	s_setprio 0
	s_add_i32 s74, 0, 0x18000
	v_add_u32_e32 v140, s74, v168
	s_barrier
	ds_read_b128 v[128:131], v140
	ds_read_b128 v[132:135], v140 offset:1024
	ds_read_b128 v[136:139], v140 offset:2048
	ds_read_b128 v[140:143], v140 offset:3072
	s_add_u32 s34, s34, 0x30000
	s_addc_u32 s35, s35, 0
	s_mov_b32 m0, s45
	v_lshl_add_u64 v[202:203], s[34:35], 0, v[144:145]
	ds_read_b128 v[158:161], v173 offset:32768
	ds_read_b128 v[162:165], v173 offset:33792
	ds_read_b128 v[178:181], v173 offset:34816
	ds_read_b128 v[182:185], v173 offset:35840
	ds_read_b128 v[186:189], v173 offset:36864
	ds_read_b128 v[190:193], v173 offset:37888
	ds_read_b128 v[194:197], v173 offset:38912
	ds_read_b128 v[198:201], v173 offset:39936
	global_load_lds_dwordx4 v[202:203], off
	v_lshl_add_u64 v[202:203], s[34:35], 0, v[148:149]
	s_mov_b32 m0, s46
	s_nop 0
	global_load_lds_dwordx4 v[202:203], off
	s_waitcnt lgkmcnt(8)
	s_barrier
	s_waitcnt lgkmcnt(0)
	s_setprio 1
	s_waitcnt lgkmcnt(0)
	v_mfma_f32_16x16x32_f16 v[124:127], v[128:131], v[158:161], v[124:127]
	v_mfma_f32_16x16x32_f16 v[120:123], v[136:139], v[158:161], v[120:123]
	v_mfma_f32_16x16x32_f16 v[108:111], v[128:131], v[178:181], v[108:111]
	v_mfma_f32_16x16x32_f16 v[104:107], v[136:139], v[178:181], v[104:107]
	v_mfma_f32_16x16x32_f16 v[96:99], v[128:131], v[186:189], v[96:99]
	v_mfma_f32_16x16x32_f16 v[88:91], v[136:139], v[186:189], v[88:91]
	v_mfma_f32_16x16x32_f16 v[80:83], v[128:131], v[194:197], v[80:83]
	v_mfma_f32_16x16x32_f16 v[72:75], v[136:139], v[194:197], v[72:75]
	v_mfma_f32_16x16x32_f16 v[124:127], v[132:135], v[162:165], v[124:127]
	v_mfma_f32_16x16x32_f16 v[120:123], v[140:143], v[162:165], v[120:123]
	v_mfma_f32_16x16x32_f16 v[108:111], v[132:135], v[182:185], v[108:111]
	v_mfma_f32_16x16x32_f16 v[104:107], v[140:143], v[182:185], v[104:107]
	v_mfma_f32_16x16x32_f16 v[96:99], v[132:135], v[190:193], v[96:99]
	v_mfma_f32_16x16x32_f16 v[88:91], v[140:143], v[190:193], v[88:91]
	v_mfma_f32_16x16x32_f16 v[80:83], v[132:135], v[198:201], v[80:83]
	v_mfma_f32_16x16x32_f16 v[72:75], v[140:143], v[198:201], v[72:75]
	s_setprio 0
	s_barrier
	s_add_i32 s34, 0, 0x1c000
	s_add_i32 s35, s74, s42
	v_add_u32_e32 v177, s34, v168
	v_lshl_add_u64 v[218:219], v[218:219], 0, s[26:27]
	s_mov_b32 m0, s35
	ds_read_b128 v[202:205], v177
	ds_read_b128 v[206:209], v177 offset:1024
	ds_read_b128 v[210:213], v177 offset:2048
	ds_read_b128 v[214:217], v177 offset:3072
	global_load_lds_dwordx4 v[218:219], off
	v_lshl_add_u64 v[218:219], v[220:221], 0, s[26:27]
	s_add_i32 m0, s35, 0x2000
	s_nop 0
	global_load_lds_dwordx4 v[218:219], off
	s_barrier
	s_waitcnt lgkmcnt(0)
	s_setprio 1
	s_waitcnt lgkmcnt(0)
	v_mfma_f32_16x16x32_f16 v[116:119], v[202:205], v[158:161], v[116:119]
	v_mfma_f32_16x16x32_f16 v[112:115], v[210:213], v[158:161], v[112:115]
	v_mfma_f32_16x16x32_f16 v[100:103], v[202:205], v[178:181], v[100:103]
	v_mfma_f32_16x16x32_f16 v[92:95], v[210:213], v[178:181], v[92:95]
	v_mfma_f32_16x16x32_f16 v[84:87], v[202:205], v[186:189], v[84:87]
	v_mfma_f32_16x16x32_f16 v[76:79], v[210:213], v[186:189], v[76:79]
	v_mfma_f32_16x16x32_f16 v[68:71], v[202:205], v[194:197], v[68:71]
	v_mfma_f32_16x16x32_f16 v[64:67], v[210:213], v[194:197], v[64:67]
	v_mfma_f32_16x16x32_f16 v[116:119], v[206:209], v[162:165], v[116:119]
	v_mfma_f32_16x16x32_f16 v[112:115], v[214:217], v[162:165], v[112:115]
	v_mfma_f32_16x16x32_f16 v[100:103], v[206:209], v[182:185], v[100:103]
	v_mfma_f32_16x16x32_f16 v[92:95], v[214:217], v[182:185], v[92:95]
	v_mfma_f32_16x16x32_f16 v[84:87], v[206:209], v[190:193], v[84:87]
	v_mfma_f32_16x16x32_f16 v[76:79], v[214:217], v[190:193], v[76:79]
	v_mfma_f32_16x16x32_f16 v[68:71], v[206:209], v[198:201], v[68:71]
	v_mfma_f32_16x16x32_f16 v[64:67], v[214:217], v[198:201], v[64:67]
	s_setprio 0
	s_mov_b32 m0, s49
	v_lshl_add_u64 v[218:219], v[222:223], 0, s[26:27]
	s_barrier
	ds_read_b128 v[158:161], v173 offset:49152
	ds_read_b128 v[162:165], v173 offset:50176
	ds_read_b128 v[178:181], v173 offset:51200
	ds_read_b128 v[182:185], v173 offset:52224
	ds_read_b128 v[186:189], v173 offset:53248
	ds_read_b128 v[190:193], v173 offset:54272
	ds_read_b128 v[194:197], v173 offset:55296
	ds_read_b128 v[198:201], v173 offset:56320
	global_load_lds_dwordx4 v[218:219], off
	v_lshl_add_u64 v[218:219], v[224:225], 0, s[26:27]
	s_mov_b32 m0, s50
	s_nop 0
	global_load_lds_dwordx4 v[218:219], off
	s_barrier
	s_waitcnt lgkmcnt(0)
	s_setprio 1
	s_waitcnt lgkmcnt(0)
	v_mfma_f32_16x16x32_f16 v[60:63], v[128:131], v[158:161], v[60:63]
	v_mfma_f32_16x16x32_f16 v[56:59], v[136:139], v[158:161], v[56:59]
	v_mfma_f32_16x16x32_f16 v[48:51], v[128:131], v[178:181], v[48:51]
	v_mfma_f32_16x16x32_f16 v[40:43], v[136:139], v[178:181], v[40:43]
	v_mfma_f32_16x16x32_f16 v[32:35], v[128:131], v[186:189], v[32:35]
	v_mfma_f32_16x16x32_f16 v[24:27], v[136:139], v[186:189], v[24:27]
	v_mfma_f32_16x16x32_f16 v[16:19], v[128:131], v[194:197], v[16:19]
	v_mfma_f32_16x16x32_f16 v[8:11], v[136:139], v[194:197], v[8:11]
	v_mfma_f32_16x16x32_f16 v[60:63], v[132:135], v[162:165], v[60:63]
	v_mfma_f32_16x16x32_f16 v[56:59], v[140:143], v[162:165], v[56:59]
	v_mfma_f32_16x16x32_f16 v[48:51], v[132:135], v[182:185], v[48:51]
	v_mfma_f32_16x16x32_f16 v[40:43], v[140:143], v[182:185], v[40:43]
	v_mfma_f32_16x16x32_f16 v[32:35], v[132:135], v[190:193], v[32:35]
	v_mfma_f32_16x16x32_f16 v[24:27], v[140:143], v[190:193], v[24:27]
	v_mfma_f32_16x16x32_f16 v[16:19], v[132:135], v[198:201], v[16:19]
	v_mfma_f32_16x16x32_f16 v[8:11], v[140:143], v[198:201], v[8:11]
	s_setprio 0
	s_barrier
	s_add_u32 s30, s30, 0xc080
	s_addc_u32 s31, s31, 0
	s_add_i32 s34, s34, s42
	v_lshl_add_u64 v[128:129], s[30:31], 0, v[146:147]
	s_mov_b32 m0, s34
	s_nop 0
	global_load_lds_dwordx4 v[128:129], off
	v_lshl_add_u64 v[128:129], s[30:31], 0, v[150:151]
	s_add_i32 m0, s34, 0x2000
	s_nop 0
	global_load_lds_dwordx4 v[128:129], off
	s_waitcnt vmcnt(6)
	s_barrier
	s_setprio 1
	v_mfma_f32_16x16x32_f16 v[52:55], v[202:205], v[158:161], v[52:55]
	v_mfma_f32_16x16x32_f16 v[44:47], v[210:213], v[158:161], v[44:47]
	v_mfma_f32_16x16x32_f16 v[36:39], v[202:205], v[178:181], v[36:39]
	v_mfma_f32_16x16x32_f16 v[28:31], v[210:213], v[178:181], v[28:31]
	v_mfma_f32_16x16x32_f16 v[20:23], v[202:205], v[186:189], v[20:23]
	v_mfma_f32_16x16x32_f16 v[12:15], v[210:213], v[186:189], v[12:15]
	v_mfma_f32_16x16x32_f16 v[4:7], v[202:205], v[194:197], v[4:7]
	v_mfma_f32_16x16x32_f16 v[0:3], v[210:213], v[194:197], v[0:3]
	v_mfma_f32_16x16x32_f16 v[52:55], v[206:209], v[162:165], v[52:55]
	v_mfma_f32_16x16x32_f16 v[44:47], v[214:217], v[162:165], v[44:47]
	v_mfma_f32_16x16x32_f16 v[36:39], v[206:209], v[182:185], v[36:39]
	v_mfma_f32_16x16x32_f16 v[28:31], v[214:217], v[182:185], v[28:31]
	v_mfma_f32_16x16x32_f16 v[20:23], v[206:209], v[190:193], v[20:23]
	v_mfma_f32_16x16x32_f16 v[12:15], v[214:217], v[190:193], v[12:15]
	v_mfma_f32_16x16x32_f16 v[4:7], v[206:209], v[198:201], v[4:7]
	v_mfma_f32_16x16x32_f16 v[0:3], v[214:217], v[198:201], v[0:3]
	s_setprio 0
	s_add_i32 s73, s73, 2
	s_add_u32 s28, s28, 0x100
	s_addc_u32 s29, s29, 0
	s_add_u32 s71, s71, 0x100
	s_addc_u32 s72, s72, 0
	s_cmp_gt_u32 s73, 9
	s_barrier
	s_cbranch_scc0 .LBB9_27
	s_lshl_b32 s28, s70, 8
	s_add_i32 s28, s28, s48
	s_lshl_b32 s29, s68, 8
	s_or_b32 s29, s29, s51
	s_waitcnt vmcnt(6)
	v_pk_fma_f32 v[126:127], v[126:127], v[226:227], v[236:237] op_sel_hi:[1,0,1]
	v_pk_fma_f32 v[124:125], v[124:125], v[226:227], v[234:235] op_sel_hi:[1,0,1]
	v_pk_fma_f32 v[122:123], v[122:123], v[226:227], v[240:241] op_sel_hi:[1,0,1]
	v_pk_fma_f32 v[120:121], v[120:121], v[226:227], v[238:239] op_sel_hi:[1,0,1]
	v_cvt_pk_f16_f32 v124, v124, v125
	v_cvt_pk_f16_f32 v125, v126, v127
	v_cvt_pk_f16_f32 v126, v120, v121
	v_cvt_pk_f16_f32 v123, v122, v123
	v_pk_fma_f32 v[118:119], v[118:119], v[226:227], v[244:245] op_sel_hi:[1,0,1]
	v_pk_fma_f32 v[116:117], v[116:117], v[226:227], v[242:243] op_sel_hi:[1,0,1]
	v_pk_fma_f32 v[114:115], v[114:115], v[226:227], v[248:249] op_sel_hi:[1,0,1]
	v_pk_fma_f32 v[112:113], v[112:113], v[226:227], v[246:247] op_sel_hi:[1,0,1]
	v_pk_max_f16 v120, v124, 0
	v_pk_max_f16 v121, v125, 0
	v_pk_max_f16 v122, v126, 0
	v_pk_max_f16 v123, v123, 0
	v_cvt_pk_f16_f32 v116, v116, v117
	v_cvt_pk_f16_f32 v117, v118, v119
	v_cvt_pk_f16_f32 v118, v112, v113
	v_cvt_pk_f16_f32 v115, v114, v115
	v_pk_fma_f32 v[110:111], v[110:111], v[226:227], v[236:237] op_sel:[0,1,0]
	v_pk_fma_f32 v[108:109], v[108:109], v[226:227], v[234:235] op_sel:[0,1,0]
	v_pk_fma_f32 v[106:107], v[106:107], v[226:227], v[240:241] op_sel:[0,1,0]
	v_pk_fma_f32 v[104:105], v[104:105], v[226:227], v[238:239] op_sel:[0,1,0]
	v_pk_fma_f32 v[102:103], v[102:103], v[226:227], v[244:245] op_sel:[0,1,0]
	v_pk_fma_f32 v[100:101], v[100:101], v[226:227], v[242:243] op_sel:[0,1,0]
	v_pk_fma_f32 v[94:95], v[94:95], v[226:227], v[248:249] op_sel:[0,1,0]
	v_pk_fma_f32 v[92:93], v[92:93], v[226:227], v[246:247] op_sel:[0,1,0]
	ds_write_b128 v175, v[120:123]
	v_or_b32_e32 v120, s28, v169
	v_pk_max_f16 v112, v116, 0
	v_pk_max_f16 v113, v117, 0
	v_pk_max_f16 v114, v118, 0
	v_pk_max_f16 v115, v115, 0
	v_cvt_pk_f16_f32 v108, v108, v109
	v_cvt_pk_f16_f32 v109, v110, v111
	v_cvt_pk_f16_f32 v110, v104, v105
	v_cvt_pk_f16_f32 v107, v106, v107
	v_cvt_pk_f16_f32 v100, v100, v101
	v_cvt_pk_f16_f32 v101, v102, v103
	v_cvt_pk_f16_f32 v102, v92, v93
	v_cvt_pk_f16_f32 v95, v94, v95
	ds_write_b128 v175, v[112:115] offset:64
	v_mul_lo_u32 v116, v120, s10
	v_pk_max_f16 v104, v108, 0
	v_pk_max_f16 v105, v109, 0
	v_pk_max_f16 v106, v110, 0
	v_pk_max_f16 v107, v107, 0
	v_pk_max_f16 v92, v100, 0
	v_pk_max_f16 v93, v101, 0
	v_pk_max_f16 v94, v102, 0
	v_pk_max_f16 v95, v95, 0
	ds_read_b128 v[112:115], v176
	v_add_u32_e32 v120, s29, v116
	ds_read_b128 v[116:119], v176 offset:1152
	ds_write_b128 v175, v[104:107]
	ds_write_b128 v175, v[92:95] offset:64
	ds_read_b128 v[92:95], v176
	ds_read_b128 v[100:103], v176 offset:1152
	v_lshlrev_b32_e32 v121, 1, v120
	v_add_u32_e32 v122, v121, v170
	v_add_u32_e32 v104, s55, v121
	s_waitcnt lgkmcnt(0)
	buffer_store_dwordx4 v[112:115], v122, s[20:23], 0 offen nt
	v_add_u32_e32 v105, v104, v170
	v_pk_fma_f32 v[90:91], v[90:91], v[228:229], v[240:241] op_sel_hi:[1,0,1]
	v_add_u32_e32 v112, v121, v171
	buffer_store_dwordx4 v[116:119], v112, s[20:23], 0 offen nt
	buffer_store_dwordx4 v[92:95], v105, s[20:23], 0 offen nt
	v_pk_fma_f32 v[88:89], v[88:89], v[228:229], v[238:239] op_sel_hi:[1,0,1]
	v_pk_fma_f32 v[86:87], v[86:87], v[228:229], v[244:245] op_sel_hi:[1,0,1]
	v_pk_fma_f32 v[92:93], v[98:99], v[228:229], v[236:237] op_sel_hi:[1,0,1]
	v_pk_fma_f32 v[94:95], v[96:97], v[228:229], v[234:235] op_sel_hi:[1,0,1]
	v_pk_fma_f32 v[84:85], v[84:85], v[228:229], v[242:243] op_sel_hi:[1,0,1]
	v_pk_fma_f32 v[78:79], v[78:79], v[228:229], v[248:249] op_sel_hi:[1,0,1]
	v_pk_fma_f32 v[76:77], v[76:77], v[228:229], v[246:247] op_sel_hi:[1,0,1]
	v_cvt_pk_f16_f32 v94, v94, v95
	v_cvt_pk_f16_f32 v92, v92, v93
	v_cvt_pk_f16_f32 v93, v88, v89
	v_cvt_pk_f16_f32 v91, v90, v91
	v_cvt_pk_f16_f32 v84, v84, v85
	v_cvt_pk_f16_f32 v85, v86, v87
	v_cvt_pk_f16_f32 v86, v76, v77
	v_cvt_pk_f16_f32 v79, v78, v79
	v_pk_max_f16 v88, v94, 0
	v_pk_max_f16 v89, v92, 0
	v_pk_max_f16 v90, v93, 0
	v_pk_max_f16 v91, v91, 0
	v_pk_max_f16 v76, v84, 0
	v_pk_max_f16 v77, v85, 0
	v_pk_max_f16 v78, v86, 0
	v_pk_max_f16 v79, v79, 0
	ds_write_b128 v175, v[88:91]
	ds_write_b128 v175, v[76:79] offset:64
	ds_read_b128 v[76:79], v176
	ds_read_b128 v[84:87], v176 offset:1152
	v_add_u32_e32 v88, s55, v104
	v_add_u32_e32 v105, v104, v171
	v_add_u32_e32 v89, v88, v170
	buffer_store_dwordx4 v[100:103], v105, s[20:23], 0 offen nt
	s_waitcnt lgkmcnt(1)
	buffer_store_dwordx4 v[76:79], v89, s[20:23], 0 offen nt
	v_pk_fma_f32 v[74:75], v[74:75], v[228:229], v[240:241] op_sel:[0,1,0]
	v_pk_fma_f32 v[72:73], v[72:73], v[228:229], v[238:239] op_sel:[0,1,0]
	v_add_u32_e32 v76, v88, v171
	s_waitcnt lgkmcnt(0)
	buffer_store_dwordx4 v[84:87], v76, s[20:23], 0 offen nt
	v_pk_fma_f32 v[76:77], v[82:83], v[228:229], v[236:237] op_sel:[0,1,0]
	v_pk_fma_f32 v[78:79], v[80:81], v[228:229], v[234:235] op_sel:[0,1,0]
	v_pk_fma_f32 v[70:71], v[70:71], v[228:229], v[244:245] op_sel:[0,1,0]
	v_pk_fma_f32 v[68:69], v[68:69], v[228:229], v[242:243] op_sel:[0,1,0]
	v_pk_fma_f32 v[66:67], v[66:67], v[228:229], v[248:249] op_sel:[0,1,0]
	v_pk_fma_f32 v[64:65], v[64:65], v[228:229], v[246:247] op_sel:[0,1,0]
	v_cvt_pk_f16_f32 v78, v78, v79
	v_cvt_pk_f16_f32 v76, v76, v77
	v_cvt_pk_f16_f32 v77, v72, v73
	v_cvt_pk_f16_f32 v75, v74, v75
	v_cvt_pk_f16_f32 v68, v68, v69
	v_cvt_pk_f16_f32 v69, v70, v71
	v_cvt_pk_f16_f32 v70, v64, v65
	v_cvt_pk_f16_f32 v67, v66, v67
	v_pk_fma_f32 v[62:63], v[62:63], v[230:231], v[236:237] op_sel_hi:[1,0,1]
	v_pk_fma_f32 v[60:61], v[60:61], v[230:231], v[234:235] op_sel_hi:[1,0,1]
	v_pk_fma_f32 v[58:59], v[58:59], v[230:231], v[240:241] op_sel_hi:[1,0,1]
	v_pk_fma_f32 v[56:57], v[56:57], v[230:231], v[238:239] op_sel_hi:[1,0,1]
	v_pk_fma_f32 v[54:55], v[54:55], v[230:231], v[244:245] op_sel_hi:[1,0,1]
	v_pk_fma_f32 v[52:53], v[52:53], v[230:231], v[242:243] op_sel_hi:[1,0,1]
	v_pk_fma_f32 v[46:47], v[46:47], v[230:231], v[248:249] op_sel_hi:[1,0,1]
	v_pk_fma_f32 v[44:45], v[44:45], v[230:231], v[246:247] op_sel_hi:[1,0,1]
	v_pk_max_f16 v72, v78, 0
	v_pk_max_f16 v73, v76, 0
	v_pk_max_f16 v74, v77, 0
	v_pk_max_f16 v75, v75, 0
	v_pk_max_f16 v64, v68, 0
	v_pk_max_f16 v65, v69, 0
	v_pk_max_f16 v66, v70, 0
	v_pk_max_f16 v67, v67, 0
	v_cvt_pk_f16_f32 v60, v60, v61
	v_cvt_pk_f16_f32 v61, v62, v63
	v_cvt_pk_f16_f32 v62, v56, v57
	v_cvt_pk_f16_f32 v59, v58, v59
	v_cvt_pk_f16_f32 v52, v52, v53
	v_cvt_pk_f16_f32 v53, v54, v55
	v_cvt_pk_f16_f32 v54, v44, v45
	v_cvt_pk_f16_f32 v47, v46, v47
	ds_write_b128 v175, v[72:75]
	ds_write_b128 v175, v[64:67] offset:64
	v_pk_max_f16 v56, v60, 0
	v_pk_max_f16 v57, v61, 0
	v_pk_max_f16 v58, v62, 0
	v_pk_max_f16 v59, v59, 0
	v_pk_max_f16 v44, v52, 0
	v_pk_max_f16 v45, v53, 0
	v_pk_max_f16 v46, v54, 0
	v_pk_max_f16 v47, v47, 0
	ds_read_b128 v[64:67], v176
	ds_read_b128 v[68:71], v176 offset:1152
	ds_write_b128 v175, v[56:59]
	ds_write_b128 v175, v[44:47] offset:64
	ds_read_b128 v[44:47], v176
	ds_read_b128 v[52:55], v176 offset:1152
	v_add_u32_e32 v72, s56, v120
	v_lshlrev_b32_e32 v73, 1, v72
	v_add_u32_e32 v74, v73, v170
	v_add_u32_e32 v56, s62, v88
	s_waitcnt lgkmcnt(5)
	buffer_store_dwordx4 v[64:67], v74, s[20:23], 0 offen nt
	v_add_u32_e32 v57, v56, v170
	v_pk_fma_f32 v[42:43], v[42:43], v[230:231], v[240:241] op_sel:[0,1,0]
	v_add_u32_e32 v64, v73, v171
	s_waitcnt lgkmcnt(4)
	buffer_store_dwordx4 v[68:71], v64, s[20:23], 0 offen nt
	s_waitcnt lgkmcnt(1)
	buffer_store_dwordx4 v[44:47], v57, s[20:23], 0 offen nt
	v_pk_fma_f32 v[40:41], v[40:41], v[230:231], v[238:239] op_sel:[0,1,0]
	v_pk_fma_f32 v[38:39], v[38:39], v[230:231], v[244:245] op_sel:[0,1,0]
	v_add_u32_e32 v44, v56, v171
	s_waitcnt lgkmcnt(0)
	buffer_store_dwordx4 v[52:55], v44, s[20:23], 0 offen nt
	v_pk_fma_f32 v[44:45], v[50:51], v[230:231], v[236:237] op_sel:[0,1,0]
	v_pk_fma_f32 v[46:47], v[48:49], v[230:231], v[234:235] op_sel:[0,1,0]
	v_pk_fma_f32 v[36:37], v[36:37], v[230:231], v[242:243] op_sel:[0,1,0]
	v_pk_fma_f32 v[30:31], v[30:31], v[230:231], v[248:249] op_sel:[0,1,0]
	v_pk_fma_f32 v[28:29], v[28:29], v[230:231], v[246:247] op_sel:[0,1,0]
	v_cvt_pk_f16_f32 v46, v46, v47
	v_cvt_pk_f16_f32 v44, v44, v45
	v_cvt_pk_f16_f32 v45, v40, v41
	v_cvt_pk_f16_f32 v43, v42, v43
	v_cvt_pk_f16_f32 v36, v36, v37
	v_cvt_pk_f16_f32 v37, v38, v39
	v_cvt_pk_f16_f32 v38, v28, v29
	v_cvt_pk_f16_f32 v31, v30, v31
	v_pk_max_f16 v40, v46, 0
	v_pk_max_f16 v41, v44, 0
	v_pk_max_f16 v42, v45, 0
	v_pk_max_f16 v43, v43, 0
	v_pk_max_f16 v28, v36, 0
	v_pk_max_f16 v29, v37, 0
	v_pk_max_f16 v30, v38, 0
	v_pk_max_f16 v31, v31, 0
	ds_write_b128 v175, v[40:43]
	ds_write_b128 v175, v[28:31] offset:64
	ds_read_b128 v[28:31], v176
	ds_read_b128 v[36:39], v176 offset:1152
	v_add_u32_e32 v40, s63, v72
	v_lshlrev_b32_e32 v41, 1, v40
	v_add_u32_e32 v42, v41, v170
	s_waitcnt lgkmcnt(1)
	buffer_store_dwordx4 v[28:31], v42, s[20:23], 0 offen nt
	v_pk_fma_f32 v[26:27], v[26:27], v[232:233], v[240:241] op_sel_hi:[1,0,1]
	v_pk_fma_f32 v[24:25], v[24:25], v[232:233], v[238:239] op_sel_hi:[1,0,1]
	v_add_u32_e32 v28, v41, v171
	s_waitcnt lgkmcnt(0)
	buffer_store_dwordx4 v[36:39], v28, s[20:23], 0 offen nt
	v_pk_fma_f32 v[28:29], v[34:35], v[232:233], v[236:237] op_sel_hi:[1,0,1]
	v_pk_fma_f32 v[30:31], v[32:33], v[232:233], v[234:235] op_sel_hi:[1,0,1]
	v_pk_fma_f32 v[22:23], v[22:23], v[232:233], v[244:245] op_sel_hi:[1,0,1]
	v_pk_fma_f32 v[20:21], v[20:21], v[232:233], v[242:243] op_sel_hi:[1,0,1]
	v_pk_fma_f32 v[14:15], v[14:15], v[232:233], v[248:249] op_sel_hi:[1,0,1]
	v_pk_fma_f32 v[12:13], v[12:13], v[232:233], v[246:247] op_sel_hi:[1,0,1]
	v_cvt_pk_f16_f32 v30, v30, v31
	v_cvt_pk_f16_f32 v28, v28, v29
	v_cvt_pk_f16_f32 v29, v24, v25
	v_cvt_pk_f16_f32 v27, v26, v27
	v_cvt_pk_f16_f32 v20, v20, v21
	v_cvt_pk_f16_f32 v21, v22, v23
	v_cvt_pk_f16_f32 v22, v12, v13
	v_cvt_pk_f16_f32 v15, v14, v15
	v_pk_max_f16 v24, v30, 0
	v_pk_max_f16 v25, v28, 0
	v_pk_max_f16 v26, v29, 0
	v_pk_max_f16 v27, v27, 0
	v_pk_max_f16 v12, v20, 0
	v_pk_max_f16 v13, v21, 0
	v_pk_max_f16 v14, v22, 0
	v_pk_max_f16 v15, v15, 0
	ds_write_b128 v175, v[24:27]
	ds_write_b128 v175, v[12:15] offset:64
	ds_read_b128 v[12:15], v176
	ds_read_b128 v[20:23], v176 offset:1152
	v_add_u32_e32 v24, s64, v40
	v_lshlrev_b32_e32 v25, 1, v24
	v_add_u32_e32 v26, v25, v170
	s_waitcnt lgkmcnt(1)
	buffer_store_dwordx4 v[12:15], v26, s[20:23], 0 offen nt
	v_pk_fma_f32 v[10:11], v[10:11], v[232:233], v[240:241] op_sel:[0,1,0]
	v_pk_fma_f32 v[8:9], v[8:9], v[232:233], v[238:239] op_sel:[0,1,0]
	v_pk_fma_f32 v[12:13], v[18:19], v[232:233], v[236:237] op_sel:[0,1,0]
	v_pk_fma_f32 v[14:15], v[16:17], v[232:233], v[234:235] op_sel:[0,1,0]
	v_pk_fma_f32 v[6:7], v[6:7], v[232:233], v[244:245] op_sel:[0,1,0]
	v_pk_fma_f32 v[4:5], v[4:5], v[232:233], v[242:243] op_sel:[0,1,0]
	v_pk_fma_f32 v[2:3], v[2:3], v[232:233], v[248:249] op_sel:[0,1,0]
	v_pk_fma_f32 v[0:1], v[0:1], v[232:233], v[246:247] op_sel:[0,1,0]
	v_cvt_pk_f16_f32 v14, v14, v15
	v_cvt_pk_f16_f32 v12, v12, v13
	v_cvt_pk_f16_f32 v13, v8, v9
	v_cvt_pk_f16_f32 v11, v10, v11
	v_cvt_pk_f16_f32 v4, v4, v5
	v_cvt_pk_f16_f32 v5, v6, v7
	v_cvt_pk_f16_f32 v6, v0, v1
	v_cvt_pk_f16_f32 v3, v2, v3
	v_pk_max_f16 v8, v14, 0
	v_pk_max_f16 v9, v12, 0
	v_pk_max_f16 v10, v13, 0
	v_pk_max_f16 v11, v11, 0
	v_pk_max_f16 v0, v4, 0
	v_pk_max_f16 v1, v5, 0
	v_pk_max_f16 v2, v6, 0
	v_pk_max_f16 v3, v3, 0
	ds_write_b128 v175, v[8:11]
	ds_write_b128 v175, v[0:3] offset:64
	ds_read_b128 v[0:3], v176
	ds_read_b128 v[4:7], v176 offset:1152
	v_add_lshl_u32 v8, v24, s64, 1
	v_add_u32_e32 v25, v25, v171
	v_add_u32_e32 v9, v8, v170
	s_waitcnt lgkmcnt(4)
	buffer_store_dwordx4 v[20:23], v25, s[20:23], 0 offen nt
	s_waitcnt lgkmcnt(1)
	buffer_store_dwordx4 v[0:3], v9, s[20:23], 0 offen nt
	s_mov_b32 s68, s67
	s_mov_b32 s70, s69
	v_add_u32_e32 v0, v8, v171
	s_mov_b64 s[30:31], s[0:1]
	s_mov_b64 s[28:29], s[8:9]
	s_mov_b64 vcc, s[6:7]
	s_waitcnt lgkmcnt(0)
	buffer_store_dwordx4 v[4:7], v0, s[20:23], 0 offen nt
	s_cbranch_vccz .LBB9_12
	s_waitcnt vmcnt(0)
	s_cmpk_gt_u32 s36, 0xff
	s_cbranch_scc1 .LBB9_31
	s_barrier

.LBB9_32:
	s_endpgm
	s_endpgm
	s_endpgm
	s_endpgm
	s_endpgm
	s_endpgm
	s_endpgm
	s_endpgm
	s_endpgm
	s_endpgm
	s_endpgm
	s_endpgm
	s_endpgm
	s_endpgm
	s_endpgm
	s_endpgm
	s_endpgm
	s_endpgm
	s_endpgm
	s_endpgm
	s_endpgm
	s_endpgm
	s_endpgm
	s_endpgm
	s_endpgm
	s_endpgm
	s_endpgm
	s_endpgm
	s_endpgm
	s_endpgm
	s_endpgm
	s_endpgm
	s_endpgm
	s_endpgm
	s_endpgm
	s_endpgm
	s_endpgm
	s_endpgm
	s_endpgm
	s_endpgm
	s_endpgm
	s_endpgm
	s_endpgm
	s_endpgm
	s_endpgm
	s_endpgm
	s_endpgm
	s_endpgm
	s_endpgm
	s_endpgm
	s_endpgm
	s_endpgm
	s_endpgm
	s_endpgm
	s_endpgm
	s_endpgm
	s_endpgm

	.amdhsa_kernel _Z6k_gemmIN2pg6EpiLinILi1EEELi768EEvNS0_4GemmET_
		.amdhsa_group_segment_fixed_size 0
		.amdhsa_private_segment_fixed_size 0
		.amdhsa_kernarg_size 320
		.amdhsa_user_sgpr_count 2
		.amdhsa_user_sgpr_dispatch_ptr 0
		.amdhsa_user_sgpr_queue_ptr 0
		.amdhsa_user_sgpr_kernarg_segment_ptr 1
		.amdhsa_user_sgpr_dispatch_id 0
		.amdhsa_user_sgpr_kernarg_preload_length 0
		.amdhsa_user_sgpr_kernarg_preload_offset 0
		.amdhsa_user_sgpr_private_segment_size 0
		.amdhsa_uses_dynamic_stack 0
		.amdhsa_enable_private_segment 0
		.amdhsa_system_sgpr_workgroup_id_x 1
		.amdhsa_system_sgpr_workgroup_id_y 0
		.amdhsa_system_sgpr_workgroup_id_z 0
		.amdhsa_system_sgpr_workgroup_info 0
		.amdhsa_system_vgpr_workitem_id 0
		.amdhsa_next_free_vgpr 254
		.amdhsa_next_free_sgpr 77
		.amdhsa_accum_offset 256
		.amdhsa_reserve_vcc 1
		.amdhsa_float_round_mode_32 0
		.amdhsa_float_round_mode_16_64 0
		.amdhsa_float_denorm_mode_32 3
		.amdhsa_float_denorm_mode_16_64 3
		.amdhsa_dx10_clamp 1
		.amdhsa_ieee_mode 1
		.amdhsa_fp16_overflow 0
		.amdhsa_tg_split 0
		.amdhsa_exception_fp_ieee_invalid_op 0
		.amdhsa_exception_fp_denorm_src 0
		.amdhsa_exception_fp_ieee_div_zero 0
		.amdhsa_exception_fp_ieee_overflow 0
		.amdhsa_exception_fp_ieee_underflow 0
		.amdhsa_exception_fp_ieee_inexact 0
		.amdhsa_exception_int_div_zero 0
	.end_amdhsa_kernel

amdhsa.kernels:
  - .agpr_count:     16
    .args:
      - .actual_access:  read_only
        .address_space:  global
        .offset:         0
        .size:           8
        .value_kind:     global_buffer
      - .actual_access:  read_only
        .address_space:  global
        .offset:         8
        .size:           8
        .value_kind:     global_buffer
      - .actual_access:  write_only
        .address_space:  global
        .offset:         16
        .size:           8
        .value_kind:     global_buffer
    .group_segment_fixed_size: 45056
    .kernarg_segment_align: 8
    .kernarg_segment_size: 24
    .language:       OpenCL C
    .language_version:
      - 2
      - 0
    .max_flat_workgroup_size: 256
    .name:           _Z6k_attnPKDF16_PKfPDF16_
    .private_segment_fixed_size: 0
    .sgpr_count:     16
    .sgpr_spill_count: 0
    .symbol:         _Z6k_attnPKDF16_PKfPDF16_.kd
    .uniform_work_group_size: 1
    .uses_dynamic_stack: false
    .vgpr_count:     84
    .vgpr_spill_count: 0
    .wavefront_size: 64
  - .agpr_count:     0
    .args:
      - .actual_access:  read_only
        .address_space:  global
        .offset:         0
        .size:           8
        .value_kind:     global_buffer
      - .actual_access:  read_only
        .address_space:  global
        .offset:         8
        .size:           8
        .value_kind:     global_buffer
      - .actual_access:  write_only
        .address_space:  global
        .offset:         16
        .size:           8
        .value_kind:     global_buffer
      - .actual_access:  write_only
        .address_space:  global
        .offset:         24
        .size:           8
        .value_kind:     global_buffer
      - .actual_access:  write_only
        .address_space:  global
        .offset:         32
        .size:           8
        .value_kind:     global_buffer
      - .actual_access:  write_only
        .address_space:  global
        .offset:         40
        .size:           8
        .value_kind:     global_buffer
    .group_segment_fixed_size: 0
    .kernarg_segment_align: 8
    .kernarg_segment_size: 48
    .language:       OpenCL C
    .language_version:
      - 2
      - 0
    .max_flat_workgroup_size: 256
    .name:           _Z11k_prep_miscPKiPKfPfPDv2_fS3_S3_
    .private_segment_fixed_size: 0
    .sgpr_count:     16
    .sgpr_spill_count: 0
    .symbol:         _Z11k_prep_miscPKiPKfPfPDv2_fS3_S3_.kd
    .uniform_work_group_size: 1
    .uses_dynamic_stack: false
    .vgpr_count:     6
    .vgpr_spill_count: 0
    .wavefront_size: 64
  - .agpr_count:     0
    .args:
      - .actual_access:  read_only
        .address_space:  global
        .offset:         0
        .size:           8
        .value_kind:     global_buffer
      - .actual_access:  write_only
        .address_space:  global
        .offset:         8
        .size:           8
        .value_kind:     global_buffer
    .group_segment_fixed_size: 0
    .kernarg_segment_align: 8
    .kernarg_segment_size: 16
    .language:       OpenCL C
    .language_version:
      - 2
      - 0
    .max_flat_workgroup_size: 256
    .name:           _Z7k_cvt_xPKfPDF16_
    .private_segment_fixed_size: 0
    .sgpr_count:     14
    .sgpr_spill_count: 0
    .symbol:         _Z7k_cvt_xPKfPDF16_.kd
    .uniform_work_group_size: 1
    .uses_dynamic_stack: false
    .vgpr_count:     12
    .vgpr_spill_count: 0
    .wavefront_size: 64
  - .agpr_count:     0
    .args:
      - .offset:         0
        .size:           176
        .value_kind:     by_value
    .group_segment_fixed_size: 9216
    .kernarg_segment_align: 8
    .kernarg_segment_size: 176
    .language:       OpenCL C
    .language_version:
      - 2
      - 0
    .max_flat_workgroup_size: 256
    .name:           _Z8k_wtrans8PrepArgs
    .private_segment_fixed_size: 0
    .sgpr_count:     44
    .sgpr_spill_count: 0
    .symbol:         _Z8k_wtrans8PrepArgs.kd
    .uniform_work_group_size: 1
    .uses_dynamic_stack: false
    .vgpr_count:     18
    .vgpr_spill_count: 0
    .wavefront_size: 64
  - .agpr_count:     0
    .args:
      - .offset:         0
        .size:           176
        .value_kind:     by_value
      - .actual_access:  read_only
        .address_space:  global
        .offset:         176
        .size:           8
        .value_kind:     global_buffer
      - .actual_access:  read_only
        .address_space:  global
        .offset:         184
        .size:           8
        .value_kind:     global_buffer
    .group_segment_fixed_size: 2048
    .kernarg_segment_align: 8
    .kernarg_segment_size: 192
    .language:       OpenCL C
    .language_version:
      - 2
      - 0
    .max_flat_workgroup_size: 256
    .name:           _Z8k_colvec8PrepArgsPKfS1_
    .private_segment_fixed_size: 0
    .sgpr_count:     38
    .sgpr_spill_count: 0
    .symbol:         _Z8k_colvec8PrepArgsPKfS1_.kd
    .uniform_work_group_size: 1
    .uses_dynamic_stack: false
    .vgpr_count:     114
    .vgpr_spill_count: 0
    .wavefront_size: 64
  - .agpr_count:     0
    .args:
      - .actual_access:  read_only
        .address_space:  global
        .offset:         0
        .size:           8
        .value_kind:     global_buffer
      - .actual_access:  write_only
        .address_space:  global
        .offset:         8
        .size:           8
        .value_kind:     global_buffer
    .group_segment_fixed_size: 0
    .kernarg_segment_align: 8
    .kernarg_segment_size: 16
    .language:       OpenCL C
    .language_version:
      - 2
      - 0
    .max_flat_workgroup_size: 256
    .name:           _Z9k_rowstatPKDv2_fPS_
    .private_segment_fixed_size: 0
    .sgpr_count:     14
    .sgpr_spill_count: 0
    .symbol:         _Z9k_rowstatPKDv2_fPS_.kd
    .uniform_work_group_size: 1
    .uses_dynamic_stack: false
    .vgpr_count:     28
    .vgpr_spill_count: 0
    .wavefront_size: 64
  - .agpr_count:     0
    .args:
      - .actual_access:  read_only
        .address_space:  global
        .offset:         0
        .size:           8
        .value_kind:     global_buffer
      - .actual_access:  read_only
        .address_space:  global
        .offset:         8
        .size:           8
        .value_kind:     global_buffer
      - .actual_access:  read_only
        .address_space:  global
        .offset:         16
        .size:           8
        .value_kind:     global_buffer
      - .actual_access:  read_only
        .address_space:  global
        .offset:         24
        .size:           8
        .value_kind:     global_buffer
      - .actual_access:  write_only
        .address_space:  global
        .offset:         32
        .size:           8
        .value_kind:     global_buffer
    .group_segment_fixed_size: 0
    .kernarg_segment_align: 8
    .kernarg_segment_size: 40
    .language:       OpenCL C
    .language_version:
      - 2
      - 0
    .max_flat_workgroup_size: 256
    .name:           _Z10k_final_lnPKDF16_PKDv2_fPKfS5_Pf
    .private_segment_fixed_size: 0
    .sgpr_count:     19
    .sgpr_spill_count: 0
    .symbol:         _Z10k_final_lnPKDF16_PKDv2_fPKfS5_Pf.kd
    .uniform_work_group_size: 1
    .uses_dynamic_stack: false
    .vgpr_count:     19
    .vgpr_spill_count: 0
    .wavefront_size: 64
  - .agpr_count:     0
    .args:
      - .offset:         0
        .size:           32
        .value_kind:     by_value
      - .offset:         32
        .size:           32
        .value_kind:     by_value
      - .offset:         64
        .size:           4
        .value_kind:     hidden_block_count_x
      - .offset:         68
        .size:           4
        .value_kind:     hidden_block_count_y
      - .offset:         72
        .size:           4
        .value_kind:     hidden_block_count_z
      - .offset:         76
        .size:           2
        .value_kind:     hidden_group_size_x
      - .offset:         78
        .size:           2
        .value_kind:     hidden_group_size_y
      - .offset:         80
        .size:           2
        .value_kind:     hidden_group_size_z
      - .offset:         82
        .size:           2
        .value_kind:     hidden_remainder_x
      - .offset:         84
        .size:           2
        .value_kind:     hidden_remainder_y
      - .offset:         86
        .size:           2
        .value_kind:     hidden_remainder_z
      - .offset:         104
        .size:           8
        .value_kind:     hidden_global_offset_x
      - .offset:         112
        .size:           8
        .value_kind:     hidden_global_offset_y
      - .offset:         120
        .size:           8
        .value_kind:     hidden_global_offset_z
      - .offset:         128
        .size:           2
        .value_kind:     hidden_grid_dims
      - .offset:         184
        .size:           4
        .value_kind:     hidden_dynamic_lds_size
    .group_segment_fixed_size: 0
    .kernarg_segment_align: 8
    .kernarg_segment_size: 320
    .language:       OpenCL C
    .language_version:
      - 2
      - 0
    .max_flat_workgroup_size: 512
    .name:           _Z6k_gemmIN2pg6EpiLinILi0EEELi768EEvNS0_4GemmET_
    .private_segment_fixed_size: 0
    .sgpr_count:     83
    .sgpr_spill_count: 0
    .symbol:         _Z6k_gemmIN2pg6EpiLinILi0EEELi768EEvNS0_4GemmET_.kd
    .uniform_work_group_size: 1
    .uses_dynamic_stack: false
    .vgpr_count:     254
    .vgpr_spill_count: 0
    .wavefront_size: 64
  - .agpr_count:     0
    .args:
      - .offset:         0
        .size:           32
        .value_kind:     by_value
      - .offset:         32
        .size:           56
        .value_kind:     by_value
      - .offset:         88
        .size:           4
        .value_kind:     hidden_block_count_x
      - .offset:         92
        .size:           4
        .value_kind:     hidden_block_count_y
      - .offset:         96
        .size:           4
        .value_kind:     hidden_block_count_z
      - .offset:         100
        .size:           2
        .value_kind:     hidden_group_size_x
      - .offset:         102
        .size:           2
        .value_kind:     hidden_group_size_y
      - .offset:         104
        .size:           2
        .value_kind:     hidden_group_size_z
      - .offset:         106
        .size:           2
        .value_kind:     hidden_remainder_x
      - .offset:         108
        .size:           2
        .value_kind:     hidden_remainder_y
      - .offset:         110
        .size:           2
        .value_kind:     hidden_remainder_z
      - .offset:         128
        .size:           8
        .value_kind:     hidden_global_offset_x
      - .offset:         136
        .size:           8
        .value_kind:     hidden_global_offset_y
      - .offset:         144
        .size:           8
        .value_kind:     hidden_global_offset_z
      - .offset:         152
        .size:           2
        .value_kind:     hidden_grid_dims
      - .offset:         208
        .size:           4
        .value_kind:     hidden_dynamic_lds_size
    .group_segment_fixed_size: 0
    .kernarg_segment_align: 8
    .kernarg_segment_size: 344
    .language:       OpenCL C
    .language_version:
      - 2
      - 0
    .max_flat_workgroup_size: 512
    .name:           _Z6k_gemmIN2pg6EpiResELi768EEvNS0_4GemmET_
    .private_segment_fixed_size: 0
    .sgpr_count:     97
    .sgpr_spill_count: 0
    .symbol:         _Z6k_gemmIN2pg6EpiResELi768EEvNS0_4GemmET_.kd
    .uniform_work_group_size: 1
    .uses_dynamic_stack: false
    .vgpr_count:     250
    .vgpr_spill_count: 0
    .wavefront_size: 64
  - .agpr_count:     0
    .args:
      - .offset:         0
        .size:           32
        .value_kind:     by_value
      - .offset:         32
        .size:           32
        .value_kind:     by_value
      - .offset:         64
        .size:           4
        .value_kind:     hidden_block_count_x
      - .offset:         68
        .size:           4
        .value_kind:     hidden_block_count_y
      - .offset:         72
        .size:           4
        .value_kind:     hidden_block_count_z
      - .offset:         76
        .size:           2
        .value_kind:     hidden_group_size_x
      - .offset:         78
        .size:           2
        .value_kind:     hidden_group_size_y
      - .offset:         80
        .size:           2
        .value_kind:     hidden_group_size_z
      - .offset:         82
        .size:           2
        .value_kind:     hidden_remainder_x
      - .offset:         84
        .size:           2
        .value_kind:     hidden_remainder_y
      - .offset:         86
        .size:           2
        .value_kind:     hidden_remainder_z
      - .offset:         104
        .size:           8
        .value_kind:     hidden_global_offset_x
      - .offset:         112
        .size:           8
        .value_kind:     hidden_global_offset_y
      - .offset:         120
        .size:           8
        .value_kind:     hidden_global_offset_z
      - .offset:         128
        .size:           2
        .value_kind:     hidden_grid_dims
      - .offset:         184
        .size:           4
        .value_kind:     hidden_dynamic_lds_size
    .group_segment_fixed_size: 0
    .kernarg_segment_align: 8
    .kernarg_segment_size: 320
    .language:       OpenCL C
    .language_version:
      - 2
      - 0
    .max_flat_workgroup_size: 512
    .name:           _Z6k_gemmIN2pg6EpiLinILi1EEELi768EEvNS0_4GemmET_
    .private_segment_fixed_size: 0
    .sgpr_count:     83
    .sgpr_spill_count: 0
    .symbol:         _Z6k_gemmIN2pg6EpiLinILi1EEELi768EEvNS0_4GemmET_.kd
    .uniform_work_group_size: 1
    .uses_dynamic_stack: false
    .vgpr_count:     254
    .vgpr_spill_count: 0
    .wavefront_size: 64
  - .agpr_count:     0
    .args:
      - .offset:         0
        .size:           32
        .value_kind:     by_value
      - .offset:         32
        .size:           56
        .value_kind:     by_value
      - .offset:         88
        .size:           4
        .value_kind:     hidden_block_count_x
      - .offset:         92
        .size:           4
        .value_kind:     hidden_block_count_y
      - .offset:         96
        .size:           4
        .value_kind:     hidden_block_count_z
      - .offset:         100
        .size:           2
        .value_kind:     hidden_group_size_x
      - .offset:         102
        .size:           2
        .value_kind:     hidden_group_size_y
      - .offset:         104
        .size:           2
        .value_kind:     hidden_group_size_z
      - .offset:         106
        .size:           2
        .value_kind:     hidden_remainder_x
      - .offset:         108
        .size:           2
        .value_kind:     hidden_remainder_y
      - .offset:         110
        .size:           2
        .value_kind:     hidden_remainder_z
      - .offset:         128
        .size:           8
        .value_kind:     hidden_global_offset_x
      - .offset:         136
        .size:           8
        .value_kind:     hidden_global_offset_y
      - .offset:         144
        .size:           8
        .value_kind:     hidden_global_offset_z
      - .offset:         152
        .size:           2
        .value_kind:     hidden_grid_dims
      - .offset:         208
        .size:           4
        .value_kind:     hidden_dynamic_lds_size
    .group_segment_fixed_size: 0
    .kernarg_segment_align: 8
    .kernarg_segment_size: 344
    .language:       OpenCL C
    .language_version:
      - 2
      - 0
    .max_flat_workgroup_size: 512
    .name:           _Z6k_gemmIN2pg6EpiResELi3072EEvNS0_4GemmET_
    .private_segment_fixed_size: 0
    .sgpr_count:     97
    .sgpr_spill_count: 0
    .symbol:         _Z6k_gemmIN2pg6EpiResELi3072EEvNS0_4GemmET_.kd
    .uniform_work_group_size: 1
    .uses_dynamic_stack: false
    .vgpr_count:     250
    .vgpr_spill_count: 0
    .wavefront_size: 64
